# GEMM K-loops: MFMA blocks contain only MFMAs (setprio pair and redundant hipcc lgkmcnt ladder removed; all ds_reads already retired by the explicit lgkmcnt(0) before the block's barrier)
# speedup vs baseline: 1.0062x; 1.0062x over previous
.LBB0_240:
	ds_read_b128 v[118:121], v210
	ds_read_b128 v[122:125], v210 offset:1024
	ds_read_b128 v[130:133], v210 offset:2048
	ds_read_b128 v[134:137], v210 offset:3072
	ds_read_b128 v[146:149], v211
	ds_read_b128 v[150:153], v211 offset:1024
	ds_read_b128 v[154:157], v211 offset:2048
	ds_read_b128 v[158:161], v211 offset:3072
	s_add_i32 s8, s0, s34
	s_sub_i32 s8, s8, s20
	s_add_i32 s5, s4, s34
	s_add_i32 s18, s8, 0x7ff80
	s_cmp_eq_u32 s3, 28
	s_cselect_b64 s[8:9], -1, 0
	s_and_b64 s[14:15], s[8:9], exec
	s_cselect_b32 s14, 0, s34
	s_mov_b32 m0, s89
	ds_read_b128 v[162:165], v212
	ds_read_b128 v[166:169], v212 offset:1024
	ds_read_b128 v[170:173], v212 offset:2048
	ds_read_b128 v[174:177], v212 offset:3072
	ds_read_b128 v[178:181], v212 offset:4096
	ds_read_b128 v[182:185], v212 offset:5120
	ds_read_b128 v[186:189], v212 offset:6144
	ds_read_b128 v[190:193], v212 offset:7168
	buffer_load_dwordx4 v195, s[20:23], s18 offen lds
	s_mov_b32 m0, s90
	s_nop 0
	buffer_load_dwordx4 v205, s[20:23], s18 offen lds
	s_waitcnt vmcnt(8)
	s_waitcnt lgkmcnt(0)
	s_barrier
	v_mfma_f32_16x16x32_bf16 v[142:145], v[118:121], v[162:165], v[142:145]
	v_mfma_f32_16x16x32_bf16 v[138:141], v[130:133], v[162:165], v[138:141]
	v_mfma_f32_16x16x32_bf16 v[110:113], v[118:121], v[170:173], v[110:113]
	v_mfma_f32_16x16x32_bf16 v[106:109], v[130:133], v[170:173], v[106:109]
	v_mfma_f32_16x16x32_bf16 v[94:97], v[118:121], v[178:181], v[94:97]
	v_mfma_f32_16x16x32_bf16 v[90:93], v[130:133], v[178:181], v[90:93]
	v_mfma_f32_16x16x32_bf16 v[78:81], v[118:121], v[186:189], v[78:81]
	v_mfma_f32_16x16x32_bf16 v[74:77], v[130:133], v[186:189], v[74:77]
	v_mfma_f32_16x16x32_bf16 v[126:129], v[146:149], v[162:165], v[126:129]
	v_mfma_f32_16x16x32_bf16 v[114:117], v[154:157], v[162:165], v[114:117]
	v_mfma_f32_16x16x32_bf16 v[102:105], v[146:149], v[170:173], v[102:105]
	v_mfma_f32_16x16x32_bf16 v[98:101], v[154:157], v[170:173], v[98:101]
	v_mfma_f32_16x16x32_bf16 v[86:89], v[146:149], v[178:181], v[86:89]
	v_mfma_f32_16x16x32_bf16 v[82:85], v[154:157], v[178:181], v[82:85]
	v_mfma_f32_16x16x32_bf16 v[70:73], v[146:149], v[186:189], v[70:73]
	v_mfma_f32_16x16x32_bf16 v[66:69], v[154:157], v[186:189], v[66:69]
	v_mfma_f32_16x16x32_bf16 v[142:145], v[122:125], v[166:169], v[142:145]
	v_mfma_f32_16x16x32_bf16 v[138:141], v[134:137], v[166:169], v[138:141]
	v_mfma_f32_16x16x32_bf16 v[110:113], v[122:125], v[174:177], v[110:113]
	v_mfma_f32_16x16x32_bf16 v[106:109], v[134:137], v[174:177], v[106:109]
	v_mfma_f32_16x16x32_bf16 v[94:97], v[122:125], v[182:185], v[94:97]
	v_mfma_f32_16x16x32_bf16 v[90:93], v[134:137], v[182:185], v[90:93]
	v_mfma_f32_16x16x32_bf16 v[78:81], v[122:125], v[190:193], v[78:81]
	v_mfma_f32_16x16x32_bf16 v[74:77], v[134:137], v[190:193], v[74:77]
	v_mfma_f32_16x16x32_bf16 v[126:129], v[150:153], v[166:169], v[126:129]
	v_mfma_f32_16x16x32_bf16 v[114:117], v[158:161], v[166:169], v[114:117]
	v_mfma_f32_16x16x32_bf16 v[102:105], v[150:153], v[174:177], v[102:105]
	v_mfma_f32_16x16x32_bf16 v[98:101], v[158:161], v[174:177], v[98:101]
	v_mfma_f32_16x16x32_bf16 v[86:89], v[150:153], v[182:185], v[86:89]
	v_mfma_f32_16x16x32_bf16 v[82:85], v[158:161], v[182:185], v[82:85]
	v_mfma_f32_16x16x32_bf16 v[70:73], v[150:153], v[190:193], v[70:73]
	v_mfma_f32_16x16x32_bf16 v[66:69], v[158:161], v[190:193], v[66:69]
	s_barrier
	s_cselect_b32 s5, s1, s5
	s_sub_i32 s5, s5, s16
	s_mov_b32 m0, s52
	s_mov_b32 s18, s22
	s_mov_b32 s19, s23
	s_add_i32 s15, s5, 0x80000
	s_and_b64 s[8:9], s[86:87], s[8:9]
	ds_read_b128 v[162:165], v212 offset:16384
	ds_read_b128 v[166:169], v212 offset:17408
	ds_read_b128 v[170:173], v212 offset:18432
	ds_read_b128 v[174:177], v212 offset:19456
	ds_read_b128 v[178:181], v212 offset:20480
	ds_read_b128 v[182:185], v212 offset:21504
	ds_read_b128 v[186:189], v212 offset:22528
	ds_read_b128 v[190:193], v212 offset:23552
	buffer_load_dwordx4 v204, s[16:19], s5 offen lds
	s_mov_b32 m0, s53
	s_and_b64 s[8:9], s[8:9], exec
	buffer_load_dwordx4 v206, s[16:19], s5 offen lds
	s_mov_b32 m0, s54
	s_cselect_b32 s8, s82, s0
	buffer_load_dwordx4 v204, s[16:19], s15 offen lds
	s_mov_b32 m0, s55
	s_add_i32 s8, s8, s14
	buffer_load_dwordx4 v206, s[16:19], s15 offen lds
	s_sub_i32 s8, s8, s20
	s_mov_b32 m0, s33
	s_nop 0
	buffer_load_dwordx4 v195, s[20:23], s8 offen lds
	s_mov_b32 m0, s56
	s_nop 0
	buffer_load_dwordx4 v205, s[20:23], s8 offen lds
	s_waitcnt vmcnt(8)
	s_waitcnt lgkmcnt(0)
	s_barrier
	v_mfma_f32_16x16x32_bf16 v[62:65], v[118:121], v[162:165], v[62:65]
	v_mfma_f32_16x16x32_bf16 v[58:61], v[130:133], v[162:165], v[58:61]
	v_mfma_f32_16x16x32_bf16 v[46:49], v[118:121], v[170:173], v[46:49]
	v_mfma_f32_16x16x32_bf16 v[42:45], v[130:133], v[170:173], v[42:45]
	v_mfma_f32_16x16x32_bf16 v[30:33], v[118:121], v[178:181], v[30:33]
	v_mfma_f32_16x16x32_bf16 v[26:29], v[130:133], v[178:181], v[26:29]
	v_mfma_f32_16x16x32_bf16 v[14:17], v[118:121], v[186:189], v[14:17]
	v_mfma_f32_16x16x32_bf16 v[10:13], v[130:133], v[186:189], v[10:13]
	v_mfma_f32_16x16x32_bf16 v[54:57], v[146:149], v[162:165], v[54:57]
	v_mfma_f32_16x16x32_bf16 v[50:53], v[154:157], v[162:165], v[50:53]
	v_mfma_f32_16x16x32_bf16 v[38:41], v[146:149], v[170:173], v[38:41]
	v_mfma_f32_16x16x32_bf16 v[34:37], v[154:157], v[170:173], v[34:37]
	v_mfma_f32_16x16x32_bf16 v[22:25], v[146:149], v[178:181], v[22:25]
	v_mfma_f32_16x16x32_bf16 v[18:21], v[154:157], v[178:181], v[18:21]
	v_mfma_f32_16x16x32_bf16 v[6:9], v[146:149], v[186:189], v[6:9]
	v_mfma_f32_16x16x32_bf16 v[2:5], v[154:157], v[186:189], v[2:5]
	v_mfma_f32_16x16x32_bf16 v[62:65], v[122:125], v[166:169], v[62:65]
	v_mfma_f32_16x16x32_bf16 v[58:61], v[134:137], v[166:169], v[58:61]
	v_mfma_f32_16x16x32_bf16 v[46:49], v[122:125], v[174:177], v[46:49]
	v_mfma_f32_16x16x32_bf16 v[42:45], v[134:137], v[174:177], v[42:45]
	v_mfma_f32_16x16x32_bf16 v[30:33], v[122:125], v[182:185], v[30:33]
	v_mfma_f32_16x16x32_bf16 v[26:29], v[134:137], v[182:185], v[26:29]
	v_mfma_f32_16x16x32_bf16 v[14:17], v[122:125], v[190:193], v[14:17]
	v_mfma_f32_16x16x32_bf16 v[10:13], v[134:137], v[190:193], v[10:13]
	v_mfma_f32_16x16x32_bf16 v[54:57], v[150:153], v[166:169], v[54:57]
	v_mfma_f32_16x16x32_bf16 v[50:53], v[158:161], v[166:169], v[50:53]
	v_mfma_f32_16x16x32_bf16 v[38:41], v[150:153], v[174:177], v[38:41]
	v_mfma_f32_16x16x32_bf16 v[34:37], v[158:161], v[174:177], v[34:37]
	v_mfma_f32_16x16x32_bf16 v[22:25], v[150:153], v[182:185], v[22:25]
	v_mfma_f32_16x16x32_bf16 v[18:21], v[158:161], v[182:185], v[18:21]
	v_mfma_f32_16x16x32_bf16 v[6:9], v[150:153], v[190:193], v[6:9]
	v_mfma_f32_16x16x32_bf16 v[2:5], v[158:161], v[190:193], v[2:5]
	s_barrier
; #define PG8_BAR __builtin_amdgcn_s_barrier()
; template <class Epi, class Sched>
; __device__ __forceinline__ void gemm_phase(LAS unsigned char* lds, const Sched& S, const Epi& E) {
;     ...
;         if (cur.vr > HALF) PG8_KLOOP(true); else PG8_KLOOP(false);
;         if constexpr (Epi::ALIGN) { if (wr == 0) PG8_BAR; }
	ds_read_b128 v[118:121], v213
	ds_read_b128 v[122:125], v213 offset:1024
	ds_read_b128 v[130:133], v213 offset:2048
	ds_read_b128 v[134:137], v213 offset:3072
	ds_read_b128 v[146:149], v214
	ds_read_b128 v[150:153], v214 offset:1024
	ds_read_b128 v[154:157], v214 offset:2048
	ds_read_b128 v[158:161], v214 offset:3072
	s_add_i32 s9, s8, 0x80000
	s_mov_b32 m0, s57
	ds_read_b128 v[162:165], v212 offset:32768
	ds_read_b128 v[166:169], v212 offset:33792
	ds_read_b128 v[170:173], v212 offset:34816
	ds_read_b128 v[174:177], v212 offset:35840
	ds_read_b128 v[178:181], v212 offset:36864
	ds_read_b128 v[182:185], v212 offset:37888
	ds_read_b128 v[186:189], v212 offset:38912
	ds_read_b128 v[190:193], v212 offset:39936
	buffer_load_dwordx4 v195, s[20:23], s9 offen lds
	s_mov_b32 m0, s58
	s_nop 0
	buffer_load_dwordx4 v205, s[20:23], s9 offen lds
	s_waitcnt vmcnt(8)
	s_waitcnt lgkmcnt(0)
	s_barrier
	v_mfma_f32_16x16x32_bf16 v[142:145], v[118:121], v[162:165], v[142:145]
	v_mfma_f32_16x16x32_bf16 v[138:141], v[130:133], v[162:165], v[138:141]
	v_mfma_f32_16x16x32_bf16 v[110:113], v[118:121], v[170:173], v[110:113]
	v_mfma_f32_16x16x32_bf16 v[106:109], v[130:133], v[170:173], v[106:109]
	v_mfma_f32_16x16x32_bf16 v[94:97], v[118:121], v[178:181], v[94:97]
	v_mfma_f32_16x16x32_bf16 v[90:93], v[130:133], v[178:181], v[90:93]
	v_mfma_f32_16x16x32_bf16 v[78:81], v[118:121], v[186:189], v[78:81]
	v_mfma_f32_16x16x32_bf16 v[74:77], v[130:133], v[186:189], v[74:77]
	v_mfma_f32_16x16x32_bf16 v[126:129], v[146:149], v[162:165], v[126:129]
	v_mfma_f32_16x16x32_bf16 v[114:117], v[154:157], v[162:165], v[114:117]
	v_mfma_f32_16x16x32_bf16 v[102:105], v[146:149], v[170:173], v[102:105]
	v_mfma_f32_16x16x32_bf16 v[98:101], v[154:157], v[170:173], v[98:101]
	v_mfma_f32_16x16x32_bf16 v[86:89], v[146:149], v[178:181], v[86:89]
	v_mfma_f32_16x16x32_bf16 v[82:85], v[154:157], v[178:181], v[82:85]
	v_mfma_f32_16x16x32_bf16 v[70:73], v[146:149], v[186:189], v[70:73]
	v_mfma_f32_16x16x32_bf16 v[66:69], v[154:157], v[186:189], v[66:69]
	v_mfma_f32_16x16x32_bf16 v[142:145], v[122:125], v[166:169], v[142:145]
	v_mfma_f32_16x16x32_bf16 v[138:141], v[134:137], v[166:169], v[138:141]
	v_mfma_f32_16x16x32_bf16 v[110:113], v[122:125], v[174:177], v[110:113]
	v_mfma_f32_16x16x32_bf16 v[106:109], v[134:137], v[174:177], v[106:109]
	v_mfma_f32_16x16x32_bf16 v[94:97], v[122:125], v[182:185], v[94:97]
	v_mfma_f32_16x16x32_bf16 v[90:93], v[134:137], v[182:185], v[90:93]
	v_mfma_f32_16x16x32_bf16 v[78:81], v[122:125], v[190:193], v[78:81]
	v_mfma_f32_16x16x32_bf16 v[74:77], v[134:137], v[190:193], v[74:77]
	v_mfma_f32_16x16x32_bf16 v[126:129], v[150:153], v[166:169], v[126:129]
	v_mfma_f32_16x16x32_bf16 v[114:117], v[158:161], v[166:169], v[114:117]
	v_mfma_f32_16x16x32_bf16 v[102:105], v[150:153], v[174:177], v[102:105]
	v_mfma_f32_16x16x32_bf16 v[98:101], v[158:161], v[174:177], v[98:101]
	v_mfma_f32_16x16x32_bf16 v[86:89], v[150:153], v[182:185], v[86:89]
	v_mfma_f32_16x16x32_bf16 v[82:85], v[158:161], v[182:185], v[82:85]
	v_mfma_f32_16x16x32_bf16 v[70:73], v[150:153], v[190:193], v[70:73]
	v_mfma_f32_16x16x32_bf16 v[66:69], v[158:161], v[190:193], v[66:69]
	s_barrier
	s_mov_b32 m0, s62
	s_add_i32 s9, s5, 0x80
	ds_read_b128 v[162:165], v212 offset:49152
	ds_read_b128 v[166:169], v212 offset:50176
	ds_read_b128 v[170:173], v212 offset:51200
	ds_read_b128 v[174:177], v212 offset:52224
	ds_read_b128 v[178:181], v212 offset:53248
	ds_read_b128 v[182:185], v212 offset:54272
	ds_read_b128 v[186:189], v212 offset:55296
	ds_read_b128 v[190:193], v212 offset:56320
	buffer_load_dwordx4 v204, s[16:19], s9 offen lds
	s_mov_b32 m0, s63
	s_add_i32 s5, s5, 0x80080
	buffer_load_dwordx4 v206, s[16:19], s9 offen lds
	s_mov_b32 m0, s75
	s_addk_i32 s8, 0x80
	buffer_load_dwordx4 v204, s[16:19], s5 offen lds
	s_mov_b32 m0, s88
	s_nop 0
	buffer_load_dwordx4 v206, s[16:19], s5 offen lds
	s_mov_b32 m0, s68
	s_nop 0
	buffer_load_dwordx4 v195, s[20:23], s8 offen lds
	s_mov_b32 m0, s69
	s_nop 0
	buffer_load_dwordx4 v205, s[20:23], s8 offen lds
	s_waitcnt vmcnt(8)
	s_waitcnt lgkmcnt(0)
	s_barrier
	v_mfma_f32_16x16x32_bf16 v[62:65], v[118:121], v[162:165], v[62:65]
	v_mfma_f32_16x16x32_bf16 v[58:61], v[130:133], v[162:165], v[58:61]
	v_mfma_f32_16x16x32_bf16 v[46:49], v[118:121], v[170:173], v[46:49]
	v_mfma_f32_16x16x32_bf16 v[42:45], v[130:133], v[170:173], v[42:45]
	v_mfma_f32_16x16x32_bf16 v[30:33], v[118:121], v[178:181], v[30:33]
	v_mfma_f32_16x16x32_bf16 v[26:29], v[130:133], v[178:181], v[26:29]
	v_mfma_f32_16x16x32_bf16 v[14:17], v[118:121], v[186:189], v[14:17]
	v_mfma_f32_16x16x32_bf16 v[10:13], v[130:133], v[186:189], v[10:13]
	v_mfma_f32_16x16x32_bf16 v[54:57], v[146:149], v[162:165], v[54:57]
	v_mfma_f32_16x16x32_bf16 v[50:53], v[154:157], v[162:165], v[50:53]
	v_mfma_f32_16x16x32_bf16 v[38:41], v[146:149], v[170:173], v[38:41]
	v_mfma_f32_16x16x32_bf16 v[34:37], v[154:157], v[170:173], v[34:37]
	v_mfma_f32_16x16x32_bf16 v[22:25], v[146:149], v[178:181], v[22:25]
	v_mfma_f32_16x16x32_bf16 v[18:21], v[154:157], v[178:181], v[18:21]
	v_mfma_f32_16x16x32_bf16 v[6:9], v[146:149], v[186:189], v[6:9]
	v_mfma_f32_16x16x32_bf16 v[2:5], v[154:157], v[186:189], v[2:5]
	v_mfma_f32_16x16x32_bf16 v[62:65], v[122:125], v[166:169], v[62:65]
	v_mfma_f32_16x16x32_bf16 v[58:61], v[134:137], v[166:169], v[58:61]
	v_mfma_f32_16x16x32_bf16 v[46:49], v[122:125], v[174:177], v[46:49]
	v_mfma_f32_16x16x32_bf16 v[42:45], v[134:137], v[174:177], v[42:45]
	v_mfma_f32_16x16x32_bf16 v[30:33], v[122:125], v[182:185], v[30:33]
	v_mfma_f32_16x16x32_bf16 v[26:29], v[134:137], v[182:185], v[26:29]
	v_mfma_f32_16x16x32_bf16 v[14:17], v[122:125], v[190:193], v[14:17]
	v_mfma_f32_16x16x32_bf16 v[10:13], v[134:137], v[190:193], v[10:13]
	v_mfma_f32_16x16x32_bf16 v[54:57], v[150:153], v[166:169], v[54:57]
	v_mfma_f32_16x16x32_bf16 v[50:53], v[158:161], v[166:169], v[50:53]
	v_mfma_f32_16x16x32_bf16 v[38:41], v[150:153], v[174:177], v[38:41]
	v_mfma_f32_16x16x32_bf16 v[34:37], v[158:161], v[174:177], v[34:37]
	v_mfma_f32_16x16x32_bf16 v[22:25], v[150:153], v[182:185], v[22:25]
	v_mfma_f32_16x16x32_bf16 v[18:21], v[158:161], v[182:185], v[18:21]
	v_mfma_f32_16x16x32_bf16 v[6:9], v[150:153], v[190:193], v[6:9]
	v_mfma_f32_16x16x32_bf16 v[2:5], v[158:161], v[190:193], v[2:5]
	s_barrier
	s_add_i32 s3, s3, 2
	s_add_u32 s34, s34, 0x100
	s_addc_u32 s35, s35, 0
	s_cmp_lt_u32 s3, 30
	s_cbranch_scc1 .LBB0_240
	s_andn2_b64 vcc, exec, s[70:71]
	s_cbranch_vccnz .LBB0_243
	s_barrier

.LBB0_816:
	ds_read_b128 v[132:135], v148
	ds_read_b128 v[136:139], v148 offset:1024
	ds_read_b128 v[154:157], v148 offset:2048
	ds_read_b128 v[158:161], v148 offset:3072
	ds_read_b128 v[162:165], v149
	ds_read_b128 v[166:169], v149 offset:1024
	ds_read_b128 v[170:173], v149 offset:2048
	ds_read_b128 v[174:177], v149 offset:3072
	s_add_i32 s6, s36, s44
	s_sub_i32 s6, s6, s16
	s_add_i32 s14, s38, s44
	s_add_i32 s15, s6, 0x7ff80
	s_cmp_eq_u32 s25, 28
	s_cselect_b64 s[8:9], -1, 0
	s_and_b64 s[6:7], s[8:9], exec
	s_cselect_b32 s37, 0, s44
	s_mov_b32 m0, s67
	ds_read_b128 v[178:181], v150
	ds_read_b128 v[182:185], v150 offset:1024
	ds_read_b128 v[186:189], v150 offset:2048
	ds_read_b128 v[190:193], v150 offset:3072
	ds_read_b128 v[196:199], v150 offset:4096
	ds_read_b128 v[200:203], v150 offset:5120
	ds_read_b128 v[204:207], v150 offset:6144
	ds_read_b128 v[208:211], v150 offset:7168
	buffer_load_dwordx4 v142, s[16:19], s15 offen lds
	s_mov_b32 m0, s68
	s_nop 0
	buffer_load_dwordx4 v144, s[16:19], s15 offen lds
	s_waitcnt vmcnt(8)
	s_waitcnt lgkmcnt(0)
	s_barrier
	v_mfma_f32_16x16x32_bf16 v[126:129], v[132:135], v[178:181], v[126:129]
	v_mfma_f32_16x16x32_bf16 v[122:125], v[154:157], v[178:181], v[122:125]
	v_mfma_f32_16x16x32_bf16 v[118:121], v[132:135], v[186:189], v[118:121]
	v_mfma_f32_16x16x32_bf16 v[114:117], v[154:157], v[186:189], v[114:117]
	v_mfma_f32_16x16x32_bf16 v[98:101], v[132:135], v[196:199], v[98:101]
	v_mfma_f32_16x16x32_bf16 v[90:93], v[154:157], v[196:199], v[90:93]
	v_mfma_f32_16x16x32_bf16 v[82:85], v[132:135], v[204:207], v[82:85]
	v_mfma_f32_16x16x32_bf16 v[74:77], v[154:157], v[204:207], v[74:77]
	v_mfma_f32_16x16x32_bf16 v[110:113], v[162:165], v[178:181], v[110:113]
	v_mfma_f32_16x16x32_bf16 v[106:109], v[170:173], v[178:181], v[106:109]
	v_mfma_f32_16x16x32_bf16 v[102:105], v[162:165], v[186:189], v[102:105]
	v_mfma_f32_16x16x32_bf16 v[94:97], v[170:173], v[186:189], v[94:97]
	v_mfma_f32_16x16x32_bf16 v[86:89], v[162:165], v[196:199], v[86:89]
	v_mfma_f32_16x16x32_bf16 v[78:81], v[170:173], v[196:199], v[78:81]
	v_mfma_f32_16x16x32_bf16 v[70:73], v[162:165], v[204:207], v[70:73]
	v_mfma_f32_16x16x32_bf16 v[66:69], v[170:173], v[204:207], v[66:69]
	v_mfma_f32_16x16x32_bf16 v[126:129], v[136:139], v[182:185], v[126:129]
	v_mfma_f32_16x16x32_bf16 v[122:125], v[158:161], v[182:185], v[122:125]
	v_mfma_f32_16x16x32_bf16 v[118:121], v[136:139], v[190:193], v[118:121]
	v_mfma_f32_16x16x32_bf16 v[114:117], v[158:161], v[190:193], v[114:117]
	v_mfma_f32_16x16x32_bf16 v[98:101], v[136:139], v[200:203], v[98:101]
	v_mfma_f32_16x16x32_bf16 v[90:93], v[158:161], v[200:203], v[90:93]
	v_mfma_f32_16x16x32_bf16 v[82:85], v[136:139], v[208:211], v[82:85]
	v_mfma_f32_16x16x32_bf16 v[74:77], v[158:161], v[208:211], v[74:77]
	v_mfma_f32_16x16x32_bf16 v[110:113], v[166:169], v[182:185], v[110:113]
	v_mfma_f32_16x16x32_bf16 v[106:109], v[174:177], v[182:185], v[106:109]
	v_mfma_f32_16x16x32_bf16 v[102:105], v[166:169], v[190:193], v[102:105]
	v_mfma_f32_16x16x32_bf16 v[94:97], v[174:177], v[190:193], v[94:97]
	v_mfma_f32_16x16x32_bf16 v[86:89], v[166:169], v[200:203], v[86:89]
	v_mfma_f32_16x16x32_bf16 v[78:81], v[174:177], v[200:203], v[78:81]
	v_mfma_f32_16x16x32_bf16 v[70:73], v[166:169], v[208:211], v[70:73]
	v_mfma_f32_16x16x32_bf16 v[66:69], v[174:177], v[208:211], v[66:69]
	s_barrier
	s_cselect_b32 s14, s23, s14
	s_sub_i32 s14, s14, s4
	s_mov_b32 m0, s52
	s_mov_b32 s6, s18
	s_mov_b32 s7, s19
	s_add_i32 s15, s14, 0x80000
	s_and_b64 s[8:9], s[30:31], s[8:9]
	ds_read_b128 v[178:181], v150 offset:16384
	ds_read_b128 v[182:185], v150 offset:17408
	ds_read_b128 v[186:189], v150 offset:18432
	ds_read_b128 v[190:193], v150 offset:19456
	ds_read_b128 v[196:199], v150 offset:20480
	ds_read_b128 v[200:203], v150 offset:21504
	ds_read_b128 v[204:207], v150 offset:22528
	ds_read_b128 v[208:211], v150 offset:23552
	buffer_load_dwordx4 v143, s[4:7], s14 offen lds
	s_mov_b32 m0, s53
	s_and_b64 s[8:9], s[8:9], exec
	buffer_load_dwordx4 v145, s[4:7], s14 offen lds
	s_mov_b32 m0, s54
	s_cselect_b32 s8, s26, s36
	buffer_load_dwordx4 v143, s[4:7], s15 offen lds
	s_mov_b32 m0, s55
	s_add_i32 s8, s8, s37
	buffer_load_dwordx4 v145, s[4:7], s15 offen lds
	s_sub_i32 s8, s8, s16
	s_mov_b32 m0, s35
	s_nop 0
	buffer_load_dwordx4 v142, s[16:19], s8 offen lds
	s_mov_b32 m0, s56
	s_nop 0
	buffer_load_dwordx4 v144, s[16:19], s8 offen lds
	s_waitcnt vmcnt(8)
	s_waitcnt lgkmcnt(0)
	s_barrier
	v_mfma_f32_16x16x32_bf16 v[62:65], v[132:135], v[178:181], v[62:65]
	v_mfma_f32_16x16x32_bf16 v[58:61], v[154:157], v[178:181], v[58:61]
	v_mfma_f32_16x16x32_bf16 v[54:57], v[132:135], v[186:189], v[54:57]
	v_mfma_f32_16x16x32_bf16 v[46:49], v[154:157], v[186:189], v[46:49]
	v_mfma_f32_16x16x32_bf16 v[38:41], v[132:135], v[196:199], v[38:41]
	v_mfma_f32_16x16x32_bf16 v[30:33], v[154:157], v[196:199], v[30:33]
	v_mfma_f32_16x16x32_bf16 v[22:25], v[132:135], v[204:207], v[22:25]
	v_mfma_f32_16x16x32_bf16 v[14:17], v[154:157], v[204:207], v[14:17]
	v_mfma_f32_16x16x32_bf16 v[50:53], v[162:165], v[178:181], v[50:53]
	v_mfma_f32_16x16x32_bf16 v[42:45], v[170:173], v[178:181], v[42:45]
	v_mfma_f32_16x16x32_bf16 v[34:37], v[162:165], v[186:189], v[34:37]
	v_mfma_f32_16x16x32_bf16 v[26:29], v[170:173], v[186:189], v[26:29]
	v_mfma_f32_16x16x32_bf16 v[18:21], v[162:165], v[196:199], v[18:21]
	v_mfma_f32_16x16x32_bf16 v[10:13], v[170:173], v[196:199], v[10:13]
	v_mfma_f32_16x16x32_bf16 v[6:9], v[162:165], v[204:207], v[6:9]
	v_mfma_f32_16x16x32_bf16 v[2:5], v[170:173], v[204:207], v[2:5]
	v_mfma_f32_16x16x32_bf16 v[62:65], v[136:139], v[182:185], v[62:65]
	v_mfma_f32_16x16x32_bf16 v[58:61], v[158:161], v[182:185], v[58:61]
	v_mfma_f32_16x16x32_bf16 v[54:57], v[136:139], v[190:193], v[54:57]
	v_mfma_f32_16x16x32_bf16 v[46:49], v[158:161], v[190:193], v[46:49]
	v_mfma_f32_16x16x32_bf16 v[38:41], v[136:139], v[200:203], v[38:41]
	v_mfma_f32_16x16x32_bf16 v[30:33], v[158:161], v[200:203], v[30:33]
	v_mfma_f32_16x16x32_bf16 v[22:25], v[136:139], v[208:211], v[22:25]
	v_mfma_f32_16x16x32_bf16 v[14:17], v[158:161], v[208:211], v[14:17]
	v_mfma_f32_16x16x32_bf16 v[50:53], v[166:169], v[182:185], v[50:53]
	v_mfma_f32_16x16x32_bf16 v[42:45], v[174:177], v[182:185], v[42:45]
	v_mfma_f32_16x16x32_bf16 v[34:37], v[166:169], v[190:193], v[34:37]
	v_mfma_f32_16x16x32_bf16 v[26:29], v[174:177], v[190:193], v[26:29]
	v_mfma_f32_16x16x32_bf16 v[18:21], v[166:169], v[200:203], v[18:21]
	v_mfma_f32_16x16x32_bf16 v[10:13], v[174:177], v[200:203], v[10:13]
	v_mfma_f32_16x16x32_bf16 v[6:9], v[166:169], v[208:211], v[6:9]
	v_mfma_f32_16x16x32_bf16 v[2:5], v[174:177], v[208:211], v[2:5]
	s_barrier
	ds_read_b128 v[132:135], v151
	ds_read_b128 v[136:139], v151 offset:1024
	ds_read_b128 v[154:157], v151 offset:2048
	ds_read_b128 v[158:161], v151 offset:3072
	ds_read_b128 v[162:165], v152
	ds_read_b128 v[166:169], v152 offset:1024
	ds_read_b128 v[170:173], v152 offset:2048
	ds_read_b128 v[174:177], v152 offset:3072
	s_add_i32 s9, s8, 0x80000
	s_mov_b32 m0, s57
	ds_read_b128 v[178:181], v150 offset:32768
	ds_read_b128 v[182:185], v150 offset:33792
	ds_read_b128 v[186:189], v150 offset:34816
	ds_read_b128 v[190:193], v150 offset:35840
	ds_read_b128 v[196:199], v150 offset:36864
	ds_read_b128 v[200:203], v150 offset:37888
	ds_read_b128 v[204:207], v150 offset:38912
	ds_read_b128 v[208:211], v150 offset:39936
	buffer_load_dwordx4 v142, s[16:19], s9 offen lds
	s_mov_b32 m0, s58
	s_nop 0
	buffer_load_dwordx4 v144, s[16:19], s9 offen lds
	s_waitcnt vmcnt(8)
	s_waitcnt lgkmcnt(0)
	s_barrier
	v_mfma_f32_16x16x32_bf16 v[126:129], v[132:135], v[178:181], v[126:129]
	v_mfma_f32_16x16x32_bf16 v[122:125], v[154:157], v[178:181], v[122:125]
	v_mfma_f32_16x16x32_bf16 v[118:121], v[132:135], v[186:189], v[118:121]
	v_mfma_f32_16x16x32_bf16 v[114:117], v[154:157], v[186:189], v[114:117]
	v_mfma_f32_16x16x32_bf16 v[98:101], v[132:135], v[196:199], v[98:101]
	v_mfma_f32_16x16x32_bf16 v[90:93], v[154:157], v[196:199], v[90:93]
	v_mfma_f32_16x16x32_bf16 v[82:85], v[132:135], v[204:207], v[82:85]
	v_mfma_f32_16x16x32_bf16 v[74:77], v[154:157], v[204:207], v[74:77]
	v_mfma_f32_16x16x32_bf16 v[110:113], v[162:165], v[178:181], v[110:113]
	v_mfma_f32_16x16x32_bf16 v[106:109], v[170:173], v[178:181], v[106:109]
	v_mfma_f32_16x16x32_bf16 v[102:105], v[162:165], v[186:189], v[102:105]
	v_mfma_f32_16x16x32_bf16 v[94:97], v[170:173], v[186:189], v[94:97]
	v_mfma_f32_16x16x32_bf16 v[86:89], v[162:165], v[196:199], v[86:89]
	v_mfma_f32_16x16x32_bf16 v[78:81], v[170:173], v[196:199], v[78:81]
	v_mfma_f32_16x16x32_bf16 v[70:73], v[162:165], v[204:207], v[70:73]
	v_mfma_f32_16x16x32_bf16 v[66:69], v[170:173], v[204:207], v[66:69]
	v_mfma_f32_16x16x32_bf16 v[126:129], v[136:139], v[182:185], v[126:129]
	v_mfma_f32_16x16x32_bf16 v[122:125], v[158:161], v[182:185], v[122:125]
	v_mfma_f32_16x16x32_bf16 v[118:121], v[136:139], v[190:193], v[118:121]
	v_mfma_f32_16x16x32_bf16 v[114:117], v[158:161], v[190:193], v[114:117]
	v_mfma_f32_16x16x32_bf16 v[98:101], v[136:139], v[200:203], v[98:101]
	v_mfma_f32_16x16x32_bf16 v[90:93], v[158:161], v[200:203], v[90:93]
	v_mfma_f32_16x16x32_bf16 v[82:85], v[136:139], v[208:211], v[82:85]
	v_mfma_f32_16x16x32_bf16 v[74:77], v[158:161], v[208:211], v[74:77]
	v_mfma_f32_16x16x32_bf16 v[110:113], v[166:169], v[182:185], v[110:113]
	v_mfma_f32_16x16x32_bf16 v[106:109], v[174:177], v[182:185], v[106:109]
	v_mfma_f32_16x16x32_bf16 v[102:105], v[166:169], v[190:193], v[102:105]
	v_mfma_f32_16x16x32_bf16 v[94:97], v[174:177], v[190:193], v[94:97]
	v_mfma_f32_16x16x32_bf16 v[86:89], v[166:169], v[200:203], v[86:89]
	v_mfma_f32_16x16x32_bf16 v[78:81], v[174:177], v[200:203], v[78:81]
	v_mfma_f32_16x16x32_bf16 v[70:73], v[166:169], v[208:211], v[70:73]
	v_mfma_f32_16x16x32_bf16 v[66:69], v[174:177], v[208:211], v[66:69]
	s_barrier
	s_mov_b32 m0, s61
	s_add_i32 s9, s14, 0x80
	ds_read_b128 v[178:181], v150 offset:49152
	ds_read_b128 v[182:185], v150 offset:50176
	ds_read_b128 v[186:189], v150 offset:51200
	ds_read_b128 v[190:193], v150 offset:52224
	ds_read_b128 v[196:199], v150 offset:53248
	ds_read_b128 v[200:203], v150 offset:54272
	ds_read_b128 v[204:207], v150 offset:55296
	ds_read_b128 v[208:211], v150 offset:56320
	buffer_load_dwordx4 v143, s[4:7], s9 offen lds
	s_mov_b32 m0, s62
	s_add_i32 s14, s14, 0x80080
	buffer_load_dwordx4 v145, s[4:7], s9 offen lds
	s_mov_b32 m0, s65
	s_addk_i32 s8, 0x80
	buffer_load_dwordx4 v143, s[4:7], s14 offen lds
	s_mov_b32 m0, s66
	s_nop 0
	buffer_load_dwordx4 v145, s[4:7], s14 offen lds
	s_mov_b32 m0, s63
	s_nop 0
	buffer_load_dwordx4 v142, s[16:19], s8 offen lds
	s_mov_b32 m0, s64
	s_nop 0
	buffer_load_dwordx4 v144, s[16:19], s8 offen lds
	s_waitcnt vmcnt(8)
	s_waitcnt lgkmcnt(0)
	s_barrier
	v_mfma_f32_16x16x32_bf16 v[62:65], v[132:135], v[178:181], v[62:65]
	v_mfma_f32_16x16x32_bf16 v[58:61], v[154:157], v[178:181], v[58:61]
	v_mfma_f32_16x16x32_bf16 v[54:57], v[132:135], v[186:189], v[54:57]
	v_mfma_f32_16x16x32_bf16 v[46:49], v[154:157], v[186:189], v[46:49]
	v_mfma_f32_16x16x32_bf16 v[38:41], v[132:135], v[196:199], v[38:41]
	v_mfma_f32_16x16x32_bf16 v[30:33], v[154:157], v[196:199], v[30:33]
	v_mfma_f32_16x16x32_bf16 v[22:25], v[132:135], v[204:207], v[22:25]
	v_mfma_f32_16x16x32_bf16 v[14:17], v[154:157], v[204:207], v[14:17]
	v_mfma_f32_16x16x32_bf16 v[50:53], v[162:165], v[178:181], v[50:53]
	v_mfma_f32_16x16x32_bf16 v[42:45], v[170:173], v[178:181], v[42:45]
	v_mfma_f32_16x16x32_bf16 v[34:37], v[162:165], v[186:189], v[34:37]
	v_mfma_f32_16x16x32_bf16 v[26:29], v[170:173], v[186:189], v[26:29]
	v_mfma_f32_16x16x32_bf16 v[18:21], v[162:165], v[196:199], v[18:21]
	v_mfma_f32_16x16x32_bf16 v[10:13], v[170:173], v[196:199], v[10:13]
	v_mfma_f32_16x16x32_bf16 v[6:9], v[162:165], v[204:207], v[6:9]
	v_mfma_f32_16x16x32_bf16 v[2:5], v[170:173], v[204:207], v[2:5]
	v_mfma_f32_16x16x32_bf16 v[62:65], v[136:139], v[182:185], v[62:65]
	v_mfma_f32_16x16x32_bf16 v[58:61], v[158:161], v[182:185], v[58:61]
	v_mfma_f32_16x16x32_bf16 v[54:57], v[136:139], v[190:193], v[54:57]
	v_mfma_f32_16x16x32_bf16 v[46:49], v[158:161], v[190:193], v[46:49]
	v_mfma_f32_16x16x32_bf16 v[38:41], v[136:139], v[200:203], v[38:41]
	v_mfma_f32_16x16x32_bf16 v[30:33], v[158:161], v[200:203], v[30:33]
	v_mfma_f32_16x16x32_bf16 v[22:25], v[136:139], v[208:211], v[22:25]
	v_mfma_f32_16x16x32_bf16 v[14:17], v[158:161], v[208:211], v[14:17]
	v_mfma_f32_16x16x32_bf16 v[50:53], v[166:169], v[182:185], v[50:53]
	v_mfma_f32_16x16x32_bf16 v[42:45], v[174:177], v[182:185], v[42:45]
	v_mfma_f32_16x16x32_bf16 v[34:37], v[166:169], v[190:193], v[34:37]
	v_mfma_f32_16x16x32_bf16 v[26:29], v[174:177], v[190:193], v[26:29]
	v_mfma_f32_16x16x32_bf16 v[18:21], v[166:169], v[200:203], v[18:21]
	v_mfma_f32_16x16x32_bf16 v[10:13], v[174:177], v[200:203], v[10:13]
	v_mfma_f32_16x16x32_bf16 v[6:9], v[166:169], v[208:211], v[6:9]
	v_mfma_f32_16x16x32_bf16 v[2:5], v[174:177], v[208:211], v[2:5]
	s_barrier
	s_add_i32 s25, s25, 2
	s_add_u32 s44, s44, 0x100
	s_addc_u32 s45, s45, 0
	s_cmp_lt_u32 s25, 30
	s_cbranch_scc1 .LBB0_816
	s_andn2_b64 vcc, exec, s[20:21]
	s_cbranch_vccnz .LBB0_819
	s_barrier

.LBB0_1238:
	v_add_u32_e32 v137, 0, v157
	v_add_u32_e32 v30, 0x10000, v137
	v_add_u32_e32 v62, 0x14000, v137
	ds_read_b128 v[6:9], v30
	ds_read_b128 v[14:17], v30 offset:1024
	ds_read_b128 v[18:21], v30 offset:2048
	ds_read_b128 v[30:33], v30 offset:3072
	ds_read_b128 v[34:37], v62
	ds_read_b128 v[46:49], v62 offset:1024
	ds_read_b128 v[50:53], v62 offset:2048
	ds_read_b128 v[62:65], v62 offset:3072
	s_add_u32 s42, s18, 0x100
	s_addc_u32 s43, s19, 0
	s_add_i32 s85, s29, s18
	s_and_b64 s[14:15], s[44:45], exec
	s_cselect_b32 s86, 0, s42
	s_add_i32 s14, s18, 0x80
	v_add_u32_e32 v153, 0, v156
	s_mov_b32 m0, s79
	ds_read_b128 v[66:69], v153
	ds_read_b128 v[78:81], v153 offset:1024
	ds_read_b128 v[82:85], v153 offset:2048
	ds_read_b128 v[94:97], v153 offset:3072
	ds_read_b128 v[98:101], v153 offset:4096
	ds_read_b128 v[106:109], v153 offset:5120
	ds_read_b128 v[114:117], v153 offset:6144
	ds_read_b128 v[138:141], v153 offset:7168
	buffer_load_dwordx4 v132, s[8:11], s14 offen lds
	s_mov_b32 m0, s80
	s_nop 0
	buffer_load_dwordx4 v134, s[8:11], s14 offen lds
	s_waitcnt vmcnt(8)
	s_waitcnt lgkmcnt(0)
	s_barrier
	v_mfma_f32_16x16x32_bf16 v[126:129], v[6:9], v[66:69], v[126:129]
	v_mfma_f32_16x16x32_bf16 v[102:105], v[6:9], v[82:85], v[102:105]
	v_mfma_f32_16x16x32_bf16 v[70:73], v[6:9], v[98:101], v[70:73]
	v_mfma_f32_16x16x32_bf16 v[6:9], v[6:9], v[114:117], v[38:41]
	v_mfma_f32_16x16x32_bf16 v[126:129], v[14:17], v[78:81], v[126:129]
	v_mfma_f32_16x16x32_bf16 v[122:125], v[18:21], v[66:69], v[122:125]
	v_mfma_f32_16x16x32_bf16 v[102:105], v[14:17], v[94:97], v[102:105]
	v_mfma_f32_16x16x32_bf16 v[90:93], v[18:21], v[82:85], v[90:93]
	v_mfma_f32_16x16x32_bf16 v[70:73], v[14:17], v[106:109], v[70:73]
	v_mfma_f32_16x16x32_bf16 v[58:61], v[18:21], v[98:101], v[58:61]
	v_mfma_f32_16x16x32_bf16 v[6:9], v[14:17], v[138:141], v[6:9]
	v_mfma_f32_16x16x32_bf16 v[14:17], v[18:21], v[114:117], v[26:29]
	v_mfma_f32_16x16x32_bf16 v[26:29], v[50:53], v[66:69], v[110:113]
	v_mfma_f32_16x16x32_bf16 v[122:125], v[30:33], v[78:81], v[122:125]
	v_mfma_f32_16x16x32_bf16 v[90:93], v[30:33], v[94:97], v[90:93]
	v_mfma_f32_16x16x32_bf16 v[58:61], v[30:33], v[106:109], v[58:61]
	v_mfma_f32_16x16x32_bf16 v[14:17], v[30:33], v[138:141], v[14:17]
	v_mfma_f32_16x16x32_bf16 v[30:33], v[62:65], v[78:81], v[26:29]
	v_mfma_f32_16x16x32_bf16 v[26:29], v[34:37], v[82:85], v[86:89]
	v_mfma_f32_16x16x32_bf16 v[18:21], v[34:37], v[66:69], v[118:121]
	v_mfma_f32_16x16x32_bf16 v[66:69], v[46:49], v[94:97], v[26:29]
	v_mfma_f32_16x16x32_bf16 v[26:29], v[50:53], v[82:85], v[74:77]
	v_mfma_f32_16x16x32_bf16 v[74:77], v[62:65], v[94:97], v[26:29]
	v_mfma_f32_16x16x32_bf16 v[26:29], v[34:37], v[98:101], v[54:57]
	v_mfma_f32_16x16x32_bf16 v[54:57], v[46:49], v[106:109], v[26:29]
	v_mfma_f32_16x16x32_bf16 v[26:29], v[50:53], v[98:101], v[42:45]
	v_mfma_f32_16x16x32_bf16 v[22:25], v[34:37], v[114:117], v[22:25]
	v_mfma_f32_16x16x32_bf16 v[10:13], v[50:53], v[114:117], v[10:13]
	v_mfma_f32_16x16x32_bf16 v[42:45], v[62:65], v[106:109], v[26:29]
	v_mfma_f32_16x16x32_bf16 v[22:25], v[46:49], v[138:141], v[22:25]
	v_mfma_f32_16x16x32_bf16 v[10:13], v[62:65], v[138:141], v[10:13]
	v_mfma_f32_16x16x32_bf16 v[18:21], v[46:49], v[78:81], v[18:21]
	s_barrier
	s_and_b64 s[14:15], s[44:45], exec
	s_cselect_b32 s14, s5, s85
	s_mov_b32 m0, s66
	s_mov_b32 s18, s10
	s_mov_b32 s19, s11
	s_sub_i32 s14, s14, s16
	buffer_load_dwordx4 v151, s[16:19], s14 offen lds
	s_mov_b32 m0, s67
	s_add_i32 s15, s14, 0x80000
	buffer_load_dwordx4 v158, s[16:19], s14 offen lds
	s_mov_b32 m0, s68
	s_nop 0
	buffer_load_dwordx4 v151, s[16:19], s15 offen lds
	s_mov_b32 m0, s69
	s_nop 0
	buffer_load_dwordx4 v158, s[16:19], s15 offen lds
	s_mov_b32 m0, s65
	s_nop 0
	buffer_load_dwordx4 v3, s[8:11], s86 offen lds
	s_mov_b32 m0, s70
	s_nop 0
	buffer_load_dwordx4 v2, s[8:11], s86 offen lds
	s_waitcnt vmcnt(8)
	s_waitcnt lgkmcnt(0)
	s_barrier
	s_barrier
	v_add_u32_e32 v38, 0x18000, v137
	ds_read_b128 v[26:29], v38
	ds_read_b128 v[34:37], v38 offset:1024
	ds_read_b128 v[46:49], v38 offset:2048
	ds_read_b128 v[50:53], v38 offset:3072
	v_add_u32_e32 v38, 0x1c000, v137
	ds_read_b128 v[62:65], v38
	ds_read_b128 v[78:81], v38 offset:1024
	ds_read_b128 v[82:85], v38 offset:2048
	ds_read_b128 v[94:97], v38 offset:3072
	s_mov_b32 m0, s71
	ds_read_b128 v[86:89], v153 offset:32768
	ds_read_b128 v[98:101], v153 offset:33792
	ds_read_b128 v[106:109], v153 offset:34816
	ds_read_b128 v[114:117], v153 offset:35840
	ds_read_b128 v[138:141], v153 offset:36864
	ds_read_b128 v[142:145], v153 offset:37888
	ds_read_b128 v[172:175], v153 offset:38912
	ds_read_b128 v[176:179], v153 offset:39936
	buffer_load_dwordx4 v5, s[8:11], s86 offen lds
	s_mov_b32 m0, s72
	s_nop 0
	buffer_load_dwordx4 v4, s[8:11], s86 offen lds
	s_waitcnt vmcnt(8)
	s_waitcnt lgkmcnt(0)
	s_barrier
	v_mfma_f32_16x16x32_bf16 v[38:41], v[26:29], v[86:89], v[126:129]
	v_mfma_f32_16x16x32_bf16 v[126:129], v[34:37], v[98:101], v[38:41]
	v_mfma_f32_16x16x32_bf16 v[38:41], v[46:49], v[86:89], v[122:125]
	v_mfma_f32_16x16x32_bf16 v[122:125], v[50:53], v[98:101], v[38:41]
	v_mfma_f32_16x16x32_bf16 v[38:41], v[26:29], v[106:109], v[102:105]
	v_mfma_f32_16x16x32_bf16 v[102:105], v[34:37], v[114:117], v[38:41]
	v_mfma_f32_16x16x32_bf16 v[38:41], v[46:49], v[106:109], v[90:93]
	v_mfma_f32_16x16x32_bf16 v[90:93], v[50:53], v[114:117], v[38:41]
	v_mfma_f32_16x16x32_bf16 v[38:41], v[26:29], v[138:141], v[70:73]
	v_mfma_f32_16x16x32_bf16 v[70:73], v[34:37], v[142:145], v[38:41]
	v_mfma_f32_16x16x32_bf16 v[38:41], v[46:49], v[138:141], v[58:61]
	v_mfma_f32_16x16x32_bf16 v[4:7], v[26:29], v[172:175], v[6:9]
	v_mfma_f32_16x16x32_bf16 v[58:61], v[50:53], v[142:145], v[38:41]
	v_mfma_f32_16x16x32_bf16 v[38:41], v[34:37], v[176:179], v[4:7]
	v_mfma_f32_16x16x32_bf16 v[4:7], v[46:49], v[172:175], v[14:17]
	v_mfma_f32_16x16x32_bf16 v[26:29], v[50:53], v[176:179], v[4:7]
	v_mfma_f32_16x16x32_bf16 v[4:7], v[62:65], v[86:89], v[18:21]
	v_mfma_f32_16x16x32_bf16 v[118:121], v[78:81], v[98:101], v[4:7]
	v_mfma_f32_16x16x32_bf16 v[4:7], v[82:85], v[86:89], v[30:33]
	v_mfma_f32_16x16x32_bf16 v[110:113], v[94:97], v[98:101], v[4:7]
	v_mfma_f32_16x16x32_bf16 v[4:7], v[62:65], v[106:109], v[66:69]
	v_mfma_f32_16x16x32_bf16 v[86:89], v[78:81], v[114:117], v[4:7]
	v_mfma_f32_16x16x32_bf16 v[4:7], v[82:85], v[106:109], v[74:77]
	v_mfma_f32_16x16x32_bf16 v[74:77], v[94:97], v[114:117], v[4:7]
	v_mfma_f32_16x16x32_bf16 v[4:7], v[62:65], v[138:141], v[54:57]
	v_mfma_f32_16x16x32_bf16 v[54:57], v[78:81], v[142:145], v[4:7]
	v_mfma_f32_16x16x32_bf16 v[4:7], v[82:85], v[138:141], v[42:45]
	v_mfma_f32_16x16x32_bf16 v[42:45], v[94:97], v[142:145], v[4:7]
	v_mfma_f32_16x16x32_bf16 v[4:7], v[62:65], v[172:175], v[22:25]
	v_mfma_f32_16x16x32_bf16 v[22:25], v[78:81], v[176:179], v[4:7]
	v_mfma_f32_16x16x32_bf16 v[4:7], v[82:85], v[172:175], v[10:13]
	v_mfma_f32_16x16x32_bf16 v[10:13], v[94:97], v[176:179], v[4:7]
	s_barrier
	s_mov_b32 m0, s73
	s_add_i32 s15, s14, 0x80
	buffer_load_dwordx4 v151, s[16:19], s15 offen lds
	s_mov_b32 m0, s74
	s_add_i32 s14, s14, 0x80080
	buffer_load_dwordx4 v158, s[16:19], s15 offen lds
	s_mov_b32 m0, s77
	s_bitset1_b32 s86, 7
	buffer_load_dwordx4 v151, s[16:19], s14 offen lds
	s_mov_b32 m0, s78
	s_nop 0
	buffer_load_dwordx4 v158, s[16:19], s14 offen lds
	s_mov_b32 m0, s75
	s_nop 0
	buffer_load_dwordx4 v3, s[8:11], s86 offen lds
	s_mov_b32 m0, s76
	s_nop 0
	buffer_load_dwordx4 v2, s[8:11], s86 offen lds
	s_waitcnt vmcnt(8)
	s_waitcnt lgkmcnt(0)
	s_barrier
	s_barrier
	s_add_i32 s39, s39, 2
	s_cmp_lt_u32 s39, 30
	s_mov_b64 s[18:19], s[42:43]
	s_cbranch_scc0 .LBB0_1241

.LBB0_1246:
	v_add_u32_e32 v141, 0, v157
	v_add_u32_e32 v153, 0x10000, v141
	ds_read_b128 v[142:145], v153
	ds_read_b128 v[172:175], v153 offset:1024
	ds_read_b128 v[176:179], v153 offset:2048
	ds_read_b128 v[180:183], v153 offset:3072
	v_add_u32_e32 v153, 0x14000, v141
	ds_read_b128 v[184:187], v153
	ds_read_b128 v[188:191], v153 offset:1024
	ds_read_b128 v[196:199], v153 offset:2048
	ds_read_b128 v[200:203], v153 offset:3072
	s_add_u32 s38, s18, 0x100
	s_addc_u32 s39, s19, 0
	s_add_i32 s85, s29, s18
	s_and_b64 s[14:15], s[42:43], exec
	s_cselect_b32 s45, 0, s38
	s_add_i32 s14, s18, 0x80
	v_add_u32_e32 v153, 0, v156
	s_mov_b32 m0, s79
	ds_read_b128 v[204:207], v153
	ds_read_b128 v[208:211], v153 offset:1024
	ds_read_b128 v[212:215], v153 offset:2048
	ds_read_b128 v[216:219], v153 offset:3072
	ds_read_b128 v[220:223], v153 offset:4096
	ds_read_b128 v[224:227], v153 offset:5120
	ds_read_b128 v[228:231], v153 offset:6144
	ds_read_b128 v[232:235], v153 offset:7168
	buffer_load_dwordx4 v132, s[8:11], s14 offen lds
	s_mov_b32 m0, s80
	s_nop 0
	buffer_load_dwordx4 v134, s[8:11], s14 offen lds
	s_waitcnt vmcnt(8)
	s_waitcnt lgkmcnt(0)
	s_barrier
	v_mfma_f32_16x16x32_bf16 v[126:129], v[142:145], v[204:207], v[126:129]
	v_mfma_f32_16x16x32_bf16 v[122:125], v[176:179], v[204:207], v[122:125]
	v_mfma_f32_16x16x32_bf16 v[102:105], v[142:145], v[212:215], v[102:105]
	v_mfma_f32_16x16x32_bf16 v[90:93], v[176:179], v[212:215], v[90:93]
	v_mfma_f32_16x16x32_bf16 v[70:73], v[142:145], v[220:223], v[70:73]
	v_mfma_f32_16x16x32_bf16 v[58:61], v[176:179], v[220:223], v[58:61]
	v_mfma_f32_16x16x32_bf16 v[38:41], v[142:145], v[228:231], v[38:41]
	v_mfma_f32_16x16x32_bf16 v[26:29], v[176:179], v[228:231], v[26:29]
	v_mfma_f32_16x16x32_bf16 v[118:121], v[184:187], v[204:207], v[118:121]
	v_mfma_f32_16x16x32_bf16 v[110:113], v[196:199], v[204:207], v[110:113]
	v_mfma_f32_16x16x32_bf16 v[86:89], v[184:187], v[212:215], v[86:89]
	v_mfma_f32_16x16x32_bf16 v[74:77], v[196:199], v[212:215], v[74:77]
	v_mfma_f32_16x16x32_bf16 v[54:57], v[184:187], v[220:223], v[54:57]
	v_mfma_f32_16x16x32_bf16 v[42:45], v[196:199], v[220:223], v[42:45]
	v_mfma_f32_16x16x32_bf16 v[22:25], v[184:187], v[228:231], v[22:25]
	v_mfma_f32_16x16x32_bf16 v[10:13], v[196:199], v[228:231], v[10:13]
	v_mfma_f32_16x16x32_bf16 v[126:129], v[172:175], v[208:211], v[126:129]
	v_mfma_f32_16x16x32_bf16 v[122:125], v[180:183], v[208:211], v[122:125]
	v_mfma_f32_16x16x32_bf16 v[102:105], v[172:175], v[216:219], v[102:105]
	v_mfma_f32_16x16x32_bf16 v[90:93], v[180:183], v[216:219], v[90:93]
	v_mfma_f32_16x16x32_bf16 v[70:73], v[172:175], v[224:227], v[70:73]
	v_mfma_f32_16x16x32_bf16 v[58:61], v[180:183], v[224:227], v[58:61]
	v_mfma_f32_16x16x32_bf16 v[38:41], v[172:175], v[232:235], v[38:41]
	v_mfma_f32_16x16x32_bf16 v[26:29], v[180:183], v[232:235], v[26:29]
	v_mfma_f32_16x16x32_bf16 v[118:121], v[188:191], v[208:211], v[118:121]
	v_mfma_f32_16x16x32_bf16 v[110:113], v[200:203], v[208:211], v[110:113]
	v_mfma_f32_16x16x32_bf16 v[86:89], v[188:191], v[216:219], v[86:89]
	v_mfma_f32_16x16x32_bf16 v[74:77], v[200:203], v[216:219], v[74:77]
	v_mfma_f32_16x16x32_bf16 v[54:57], v[188:191], v[224:227], v[54:57]
	v_mfma_f32_16x16x32_bf16 v[42:45], v[200:203], v[224:227], v[42:45]
	v_mfma_f32_16x16x32_bf16 v[22:25], v[188:191], v[232:235], v[22:25]
	v_mfma_f32_16x16x32_bf16 v[10:13], v[200:203], v[232:235], v[10:13]
	s_barrier
	s_and_b64 s[14:15], s[42:43], exec
	s_cselect_b32 s14, s5, s85
	s_mov_b32 m0, s66
	s_mov_b32 s18, s10
	s_mov_b32 s19, s11
	s_sub_i32 s14, s14, s16
	ds_read_b128 v[204:207], v153 offset:16384
	ds_read_b128 v[208:211], v153 offset:17408
	ds_read_b128 v[212:215], v153 offset:18432
	ds_read_b128 v[216:219], v153 offset:19456
	ds_read_b128 v[220:223], v153 offset:20480
	ds_read_b128 v[224:227], v153 offset:21504
	ds_read_b128 v[228:231], v153 offset:22528
	ds_read_b128 v[232:235], v153 offset:23552
	buffer_load_dwordx4 v151, s[16:19], s14 offen lds
	s_mov_b32 m0, s67
	s_add_i32 s15, s14, 0x80000
	buffer_load_dwordx4 v158, s[16:19], s14 offen lds
	s_mov_b32 m0, s68
	s_nop 0
	buffer_load_dwordx4 v151, s[16:19], s15 offen lds
	s_mov_b32 m0, s69
	s_nop 0
	buffer_load_dwordx4 v158, s[16:19], s15 offen lds
	s_mov_b32 m0, s65
	s_nop 0
	buffer_load_dwordx4 v138, s[8:11], s45 offen lds
	s_mov_b32 m0, s70
	s_nop 0
	buffer_load_dwordx4 v137, s[8:11], s45 offen lds
	s_waitcnt vmcnt(8)
	s_waitcnt lgkmcnt(0)
	s_barrier
	v_mfma_f32_16x16x32_bf16 v[114:117], v[142:145], v[204:207], v[114:117]
	v_mfma_f32_16x16x32_bf16 v[98:101], v[176:179], v[204:207], v[98:101]
	v_mfma_f32_16x16x32_bf16 v[82:85], v[142:145], v[212:215], v[82:85]
	v_mfma_f32_16x16x32_bf16 v[66:69], v[176:179], v[212:215], v[66:69]
	v_mfma_f32_16x16x32_bf16 v[50:53], v[142:145], v[220:223], v[50:53]
	v_mfma_f32_16x16x32_bf16 v[34:37], v[176:179], v[220:223], v[34:37]
	v_mfma_f32_16x16x32_bf16 v[18:21], v[142:145], v[228:231], v[18:21]
	v_mfma_f32_16x16x32_bf16 v[6:9], v[176:179], v[228:231], v[6:9]
	v_mfma_f32_16x16x32_bf16 v[106:109], v[184:187], v[204:207], v[106:109]
	v_mfma_f32_16x16x32_bf16 v[94:97], v[196:199], v[204:207], v[94:97]
	v_mfma_f32_16x16x32_bf16 v[78:81], v[184:187], v[212:215], v[78:81]
	v_mfma_f32_16x16x32_bf16 v[62:65], v[196:199], v[212:215], v[62:65]
	v_mfma_f32_16x16x32_bf16 v[46:49], v[184:187], v[220:223], v[46:49]
	v_mfma_f32_16x16x32_bf16 v[30:33], v[196:199], v[220:223], v[30:33]
	v_mfma_f32_16x16x32_bf16 v[14:17], v[184:187], v[228:231], v[14:17]
	v_mfma_f32_16x16x32_bf16 v[2:5], v[196:199], v[228:231], v[2:5]
	v_mfma_f32_16x16x32_bf16 v[114:117], v[172:175], v[208:211], v[114:117]
	v_mfma_f32_16x16x32_bf16 v[98:101], v[180:183], v[208:211], v[98:101]
	v_mfma_f32_16x16x32_bf16 v[82:85], v[172:175], v[216:219], v[82:85]
	v_mfma_f32_16x16x32_bf16 v[66:69], v[180:183], v[216:219], v[66:69]
	v_mfma_f32_16x16x32_bf16 v[50:53], v[172:175], v[224:227], v[50:53]
	v_mfma_f32_16x16x32_bf16 v[34:37], v[180:183], v[224:227], v[34:37]
	v_mfma_f32_16x16x32_bf16 v[18:21], v[172:175], v[232:235], v[18:21]
	v_mfma_f32_16x16x32_bf16 v[6:9], v[180:183], v[232:235], v[6:9]
	v_mfma_f32_16x16x32_bf16 v[106:109], v[188:191], v[208:211], v[106:109]
	v_mfma_f32_16x16x32_bf16 v[94:97], v[200:203], v[208:211], v[94:97]
	v_mfma_f32_16x16x32_bf16 v[78:81], v[188:191], v[216:219], v[78:81]
	v_mfma_f32_16x16x32_bf16 v[62:65], v[200:203], v[216:219], v[62:65]
	v_mfma_f32_16x16x32_bf16 v[46:49], v[188:191], v[224:227], v[46:49]
	v_mfma_f32_16x16x32_bf16 v[30:33], v[200:203], v[224:227], v[30:33]
	v_mfma_f32_16x16x32_bf16 v[14:17], v[188:191], v[232:235], v[14:17]
	v_mfma_f32_16x16x32_bf16 v[2:5], v[200:203], v[232:235], v[2:5]
	s_barrier
	v_add_u32_e32 v154, 0x18000, v141
	v_add_u32_e32 v141, 0x1c000, v141
	ds_read_b128 v[142:145], v154
	ds_read_b128 v[172:175], v154 offset:1024
	ds_read_b128 v[176:179], v154 offset:2048
	ds_read_b128 v[180:183], v154 offset:3072
	ds_read_b128 v[184:187], v141
	ds_read_b128 v[188:191], v141 offset:1024
	ds_read_b128 v[196:199], v141 offset:2048
	ds_read_b128 v[200:203], v141 offset:3072
	s_mov_b32 m0, s71
	ds_read_b128 v[204:207], v153 offset:32768
	ds_read_b128 v[208:211], v153 offset:33792
	ds_read_b128 v[212:215], v153 offset:34816
	ds_read_b128 v[216:219], v153 offset:35840
	ds_read_b128 v[220:223], v153 offset:36864
	ds_read_b128 v[224:227], v153 offset:37888
	ds_read_b128 v[228:231], v153 offset:38912
	ds_read_b128 v[232:235], v153 offset:39936
	buffer_load_dwordx4 v140, s[8:11], s45 offen lds
	s_mov_b32 m0, s72
	s_nop 0
	buffer_load_dwordx4 v139, s[8:11], s45 offen lds
	s_waitcnt vmcnt(8)
	s_waitcnt lgkmcnt(0)
	s_barrier
	v_mfma_f32_16x16x32_bf16 v[126:129], v[142:145], v[204:207], v[126:129]
	v_mfma_f32_16x16x32_bf16 v[122:125], v[176:179], v[204:207], v[122:125]
	v_mfma_f32_16x16x32_bf16 v[102:105], v[142:145], v[212:215], v[102:105]
	v_mfma_f32_16x16x32_bf16 v[90:93], v[176:179], v[212:215], v[90:93]
	v_mfma_f32_16x16x32_bf16 v[70:73], v[142:145], v[220:223], v[70:73]
	v_mfma_f32_16x16x32_bf16 v[58:61], v[176:179], v[220:223], v[58:61]
	v_mfma_f32_16x16x32_bf16 v[38:41], v[142:145], v[228:231], v[38:41]
	v_mfma_f32_16x16x32_bf16 v[26:29], v[176:179], v[228:231], v[26:29]
	v_mfma_f32_16x16x32_bf16 v[118:121], v[184:187], v[204:207], v[118:121]
	v_mfma_f32_16x16x32_bf16 v[110:113], v[196:199], v[204:207], v[110:113]
	v_mfma_f32_16x16x32_bf16 v[86:89], v[184:187], v[212:215], v[86:89]
	v_mfma_f32_16x16x32_bf16 v[74:77], v[196:199], v[212:215], v[74:77]
	v_mfma_f32_16x16x32_bf16 v[54:57], v[184:187], v[220:223], v[54:57]
	v_mfma_f32_16x16x32_bf16 v[42:45], v[196:199], v[220:223], v[42:45]
	v_mfma_f32_16x16x32_bf16 v[22:25], v[184:187], v[228:231], v[22:25]
	v_mfma_f32_16x16x32_bf16 v[10:13], v[196:199], v[228:231], v[10:13]
	v_mfma_f32_16x16x32_bf16 v[126:129], v[172:175], v[208:211], v[126:129]
	v_mfma_f32_16x16x32_bf16 v[122:125], v[180:183], v[208:211], v[122:125]
	v_mfma_f32_16x16x32_bf16 v[102:105], v[172:175], v[216:219], v[102:105]
	v_mfma_f32_16x16x32_bf16 v[90:93], v[180:183], v[216:219], v[90:93]
	v_mfma_f32_16x16x32_bf16 v[70:73], v[172:175], v[224:227], v[70:73]
	v_mfma_f32_16x16x32_bf16 v[58:61], v[180:183], v[224:227], v[58:61]
	v_mfma_f32_16x16x32_bf16 v[38:41], v[172:175], v[232:235], v[38:41]
	v_mfma_f32_16x16x32_bf16 v[26:29], v[180:183], v[232:235], v[26:29]
	v_mfma_f32_16x16x32_bf16 v[118:121], v[188:191], v[208:211], v[118:121]
	v_mfma_f32_16x16x32_bf16 v[110:113], v[200:203], v[208:211], v[110:113]
	v_mfma_f32_16x16x32_bf16 v[86:89], v[188:191], v[216:219], v[86:89]
	v_mfma_f32_16x16x32_bf16 v[74:77], v[200:203], v[216:219], v[74:77]
	v_mfma_f32_16x16x32_bf16 v[54:57], v[188:191], v[224:227], v[54:57]
	v_mfma_f32_16x16x32_bf16 v[42:45], v[200:203], v[224:227], v[42:45]
	v_mfma_f32_16x16x32_bf16 v[22:25], v[188:191], v[232:235], v[22:25]
	v_mfma_f32_16x16x32_bf16 v[10:13], v[200:203], v[232:235], v[10:13]
	s_barrier
	s_mov_b32 m0, s73
	s_add_i32 s15, s14, 0x80
	ds_read_b128 v[204:207], v153 offset:49152
	ds_read_b128 v[208:211], v153 offset:50176
	ds_read_b128 v[212:215], v153 offset:51200
	ds_read_b128 v[216:219], v153 offset:52224
	ds_read_b128 v[220:223], v153 offset:53248
	ds_read_b128 v[224:227], v153 offset:54272
	ds_read_b128 v[228:231], v153 offset:55296
	ds_read_b128 v[232:235], v153 offset:56320
	buffer_load_dwordx4 v151, s[16:19], s15 offen lds
	s_mov_b32 m0, s74
	s_add_i32 s14, s14, 0x80080
	buffer_load_dwordx4 v158, s[16:19], s15 offen lds
	s_mov_b32 m0, s77
	s_bitset1_b32 s45, 7
	buffer_load_dwordx4 v151, s[16:19], s14 offen lds
	s_mov_b32 m0, s78
	s_nop 0
	buffer_load_dwordx4 v158, s[16:19], s14 offen lds
	s_mov_b32 m0, s75
	s_nop 0
	buffer_load_dwordx4 v138, s[8:11], s45 offen lds
	s_mov_b32 m0, s76
	s_nop 0
	buffer_load_dwordx4 v137, s[8:11], s45 offen lds
	s_waitcnt vmcnt(8)
	s_waitcnt lgkmcnt(0)
	s_barrier
	v_mfma_f32_16x16x32_bf16 v[114:117], v[142:145], v[204:207], v[114:117]
	v_mfma_f32_16x16x32_bf16 v[98:101], v[176:179], v[204:207], v[98:101]
	v_mfma_f32_16x16x32_bf16 v[82:85], v[142:145], v[212:215], v[82:85]
	v_mfma_f32_16x16x32_bf16 v[66:69], v[176:179], v[212:215], v[66:69]
	v_mfma_f32_16x16x32_bf16 v[50:53], v[142:145], v[220:223], v[50:53]
	v_mfma_f32_16x16x32_bf16 v[34:37], v[176:179], v[220:223], v[34:37]
	v_mfma_f32_16x16x32_bf16 v[18:21], v[142:145], v[228:231], v[18:21]
	v_mfma_f32_16x16x32_bf16 v[6:9], v[176:179], v[228:231], v[6:9]
	v_mfma_f32_16x16x32_bf16 v[106:109], v[184:187], v[204:207], v[106:109]
	v_mfma_f32_16x16x32_bf16 v[94:97], v[196:199], v[204:207], v[94:97]
	v_mfma_f32_16x16x32_bf16 v[78:81], v[184:187], v[212:215], v[78:81]
	v_mfma_f32_16x16x32_bf16 v[62:65], v[196:199], v[212:215], v[62:65]
	v_mfma_f32_16x16x32_bf16 v[46:49], v[184:187], v[220:223], v[46:49]
	v_mfma_f32_16x16x32_bf16 v[30:33], v[196:199], v[220:223], v[30:33]
	v_mfma_f32_16x16x32_bf16 v[14:17], v[184:187], v[228:231], v[14:17]
	v_mfma_f32_16x16x32_bf16 v[2:5], v[196:199], v[228:231], v[2:5]
	v_mfma_f32_16x16x32_bf16 v[114:117], v[172:175], v[208:211], v[114:117]
	v_mfma_f32_16x16x32_bf16 v[98:101], v[180:183], v[208:211], v[98:101]
	v_mfma_f32_16x16x32_bf16 v[82:85], v[172:175], v[216:219], v[82:85]
	v_mfma_f32_16x16x32_bf16 v[66:69], v[180:183], v[216:219], v[66:69]
	v_mfma_f32_16x16x32_bf16 v[50:53], v[172:175], v[224:227], v[50:53]
	v_mfma_f32_16x16x32_bf16 v[34:37], v[180:183], v[224:227], v[34:37]
	v_mfma_f32_16x16x32_bf16 v[18:21], v[172:175], v[232:235], v[18:21]
	v_mfma_f32_16x16x32_bf16 v[6:9], v[180:183], v[232:235], v[6:9]
	v_mfma_f32_16x16x32_bf16 v[106:109], v[188:191], v[208:211], v[106:109]
	v_mfma_f32_16x16x32_bf16 v[94:97], v[200:203], v[208:211], v[94:97]
	v_mfma_f32_16x16x32_bf16 v[78:81], v[188:191], v[216:219], v[78:81]
	v_mfma_f32_16x16x32_bf16 v[62:65], v[200:203], v[216:219], v[62:65]
	v_mfma_f32_16x16x32_bf16 v[46:49], v[188:191], v[224:227], v[46:49]
	v_mfma_f32_16x16x32_bf16 v[30:33], v[200:203], v[224:227], v[30:33]
	v_mfma_f32_16x16x32_bf16 v[14:17], v[188:191], v[232:235], v[14:17]
	v_mfma_f32_16x16x32_bf16 v[2:5], v[200:203], v[232:235], v[2:5]
	s_barrier
	s_add_i32 s44, s44, 2
	s_cmp_gt_u32 s44, 29
	s_cbranch_scc1 .LBB0_1248
	s_mov_b64 s[18:19], s[38:39]
	s_branch .LBB0_1244

.LBB0_1456:
	ds_read_b128 v[66:69], v159
	ds_read_b128 v[70:73], v159 offset:1024
	ds_read_b128 v[74:77], v159 offset:2048
	ds_read_b128 v[78:81], v159 offset:3072
	ds_read_b128 v[82:85], v160
	ds_read_b128 v[86:89], v160 offset:1024
	ds_read_b128 v[90:93], v160 offset:2048
	ds_read_b128 v[94:97], v160 offset:3072
	s_add_i32 s10, s44, s48
	s_sub_i32 s10, s10, s4
	s_add_i32 s47, s46, s48
	s_add_i32 s10, s10, 0x7ff80
	s_cmp_eq_u32 s45, 28
	s_cselect_b32 s50, 0, s48
	s_mov_b32 m0, s67
	ds_read_b128 v[98:101], v161
	ds_read_b128 v[102:105], v161 offset:1024
	ds_read_b128 v[106:109], v161 offset:2048
	ds_read_b128 v[110:113], v161 offset:3072
	ds_read_b128 v[114:117], v161 offset:4096
	ds_read_b128 v[118:121], v161 offset:5120
	ds_read_b128 v[122:125], v161 offset:6144
	ds_read_b128 v[126:129], v161 offset:7168
	buffer_load_dwordx4 v1, s[4:7], s10 offen lds
	s_mov_b32 m0, s68
	s_nop 0
	buffer_load_dwordx4 v153, s[4:7], s10 offen lds
	s_waitcnt vmcnt(8)
	s_waitcnt lgkmcnt(0)
	s_barrier
	v_mfma_f32_16x16x32_bf16 v[62:65], v[66:69], v[98:101], v[62:65]
	v_mfma_f32_16x16x32_bf16 v[58:61], v[74:77], v[98:101], v[58:61]
	v_mfma_f32_16x16x32_bf16 v[54:57], v[66:69], v[106:109], v[54:57]
	v_mfma_f32_16x16x32_bf16 v[50:53], v[74:77], v[106:109], v[50:53]
	v_mfma_f32_16x16x32_bf16 v[38:41], v[66:69], v[114:117], v[38:41]
	v_mfma_f32_16x16x32_bf16 v[34:37], v[74:77], v[114:117], v[34:37]
	v_mfma_f32_16x16x32_bf16 v[22:25], v[66:69], v[122:125], v[22:25]
	v_mfma_f32_16x16x32_bf16 v[18:21], v[74:77], v[122:125], v[18:21]
	v_mfma_f32_16x16x32_bf16 v[46:49], v[82:85], v[98:101], v[46:49]
	v_mfma_f32_16x16x32_bf16 v[42:45], v[90:93], v[98:101], v[42:45]
	v_mfma_f32_16x16x32_bf16 v[30:33], v[82:85], v[106:109], v[30:33]
	v_mfma_f32_16x16x32_bf16 v[26:29], v[90:93], v[106:109], v[26:29]
	v_mfma_f32_16x16x32_bf16 v[14:17], v[82:85], v[114:117], v[14:17]
	v_mfma_f32_16x16x32_bf16 v[10:13], v[90:93], v[114:117], v[10:13]
	v_mfma_f32_16x16x32_bf16 v[6:9], v[82:85], v[122:125], v[6:9]
	v_mfma_f32_16x16x32_bf16 v[2:5], v[90:93], v[122:125], v[2:5]
	v_mfma_f32_16x16x32_bf16 v[62:65], v[70:73], v[102:105], v[62:65]
	v_mfma_f32_16x16x32_bf16 v[58:61], v[78:81], v[102:105], v[58:61]
	v_mfma_f32_16x16x32_bf16 v[54:57], v[70:73], v[110:113], v[54:57]
	v_mfma_f32_16x16x32_bf16 v[50:53], v[78:81], v[110:113], v[50:53]
	v_mfma_f32_16x16x32_bf16 v[38:41], v[70:73], v[118:121], v[38:41]
	v_mfma_f32_16x16x32_bf16 v[34:37], v[78:81], v[118:121], v[34:37]
	v_mfma_f32_16x16x32_bf16 v[22:25], v[70:73], v[126:129], v[22:25]
	v_mfma_f32_16x16x32_bf16 v[18:21], v[78:81], v[126:129], v[18:21]
	v_mfma_f32_16x16x32_bf16 v[46:49], v[86:89], v[102:105], v[46:49]
	v_mfma_f32_16x16x32_bf16 v[42:45], v[94:97], v[102:105], v[42:45]
	v_mfma_f32_16x16x32_bf16 v[30:33], v[86:89], v[110:113], v[30:33]
	v_mfma_f32_16x16x32_bf16 v[26:29], v[94:97], v[110:113], v[26:29]
	v_mfma_f32_16x16x32_bf16 v[14:17], v[86:89], v[118:121], v[14:17]
	v_mfma_f32_16x16x32_bf16 v[10:13], v[94:97], v[118:121], v[10:13]
	v_mfma_f32_16x16x32_bf16 v[6:9], v[86:89], v[126:129], v[6:9]
	v_mfma_f32_16x16x32_bf16 v[2:5], v[94:97], v[126:129], v[2:5]
	s_barrier
	s_cselect_b32 s47, s31, s47
	s_mov_b32 m0, s53
	s_mov_b32 s10, s6
	s_mov_b32 s11, s7
	s_cselect_b32 s51, s27, s44
	s_sub_i32 s47, s47, s8
	buffer_load_dwordx4 v152, s[8:11], s47 offen lds
	s_mov_b32 m0, s54
	s_add_i32 s73, s47, 0x80000
	buffer_load_dwordx4 v154, s[8:11], s47 offen lds
	s_mov_b32 m0, s55
	s_add_i32 s51, s51, s50
	buffer_load_dwordx4 v152, s[8:11], s73 offen lds
	s_mov_b32 m0, s56
	s_sub_i32 s50, s51, s4
	buffer_load_dwordx4 v154, s[8:11], s73 offen lds
	s_mov_b32 m0, s43
	s_nop 0
	buffer_load_dwordx4 v1, s[4:7], s50 offen lds
	s_mov_b32 m0, s57
	s_nop 0
	buffer_load_dwordx4 v153, s[4:7], s50 offen lds
	s_waitcnt vmcnt(8)
	s_waitcnt lgkmcnt(0)
	s_barrier
	s_barrier
	ds_read_b128 v[66:69], v162
	ds_read_b128 v[70:73], v162 offset:1024
	ds_read_b128 v[74:77], v162 offset:2048
	ds_read_b128 v[78:81], v162 offset:3072
	ds_read_b128 v[82:85], v163
	ds_read_b128 v[86:89], v163 offset:1024
	ds_read_b128 v[90:93], v163 offset:2048
	ds_read_b128 v[94:97], v163 offset:3072
	s_add_i32 s51, s50, 0x80000
	s_mov_b32 m0, s58
	ds_read_b128 v[98:101], v161 offset:32768
	ds_read_b128 v[102:105], v161 offset:33792
	ds_read_b128 v[106:109], v161 offset:34816
	ds_read_b128 v[110:113], v161 offset:35840
	ds_read_b128 v[114:117], v161 offset:36864
	ds_read_b128 v[118:121], v161 offset:37888
	ds_read_b128 v[122:125], v161 offset:38912
	ds_read_b128 v[126:129], v161 offset:39936
	buffer_load_dwordx4 v1, s[4:7], s51 offen lds
	s_mov_b32 m0, s59
	s_nop 0
	buffer_load_dwordx4 v153, s[4:7], s51 offen lds
	s_waitcnt vmcnt(8)
	s_waitcnt lgkmcnt(0)
	s_barrier
	v_mfma_f32_16x16x32_bf16 v[62:65], v[66:69], v[98:101], v[62:65]
	v_mfma_f32_16x16x32_bf16 v[58:61], v[74:77], v[98:101], v[58:61]
	v_mfma_f32_16x16x32_bf16 v[54:57], v[66:69], v[106:109], v[54:57]
	v_mfma_f32_16x16x32_bf16 v[50:53], v[74:77], v[106:109], v[50:53]
	v_mfma_f32_16x16x32_bf16 v[38:41], v[66:69], v[114:117], v[38:41]
	v_mfma_f32_16x16x32_bf16 v[34:37], v[74:77], v[114:117], v[34:37]
	v_mfma_f32_16x16x32_bf16 v[22:25], v[66:69], v[122:125], v[22:25]
	v_mfma_f32_16x16x32_bf16 v[18:21], v[74:77], v[122:125], v[18:21]
	v_mfma_f32_16x16x32_bf16 v[46:49], v[82:85], v[98:101], v[46:49]
	v_mfma_f32_16x16x32_bf16 v[42:45], v[90:93], v[98:101], v[42:45]
	v_mfma_f32_16x16x32_bf16 v[30:33], v[82:85], v[106:109], v[30:33]
	v_mfma_f32_16x16x32_bf16 v[26:29], v[90:93], v[106:109], v[26:29]
	v_mfma_f32_16x16x32_bf16 v[14:17], v[82:85], v[114:117], v[14:17]
	v_mfma_f32_16x16x32_bf16 v[10:13], v[90:93], v[114:117], v[10:13]
	v_mfma_f32_16x16x32_bf16 v[6:9], v[82:85], v[122:125], v[6:9]
	v_mfma_f32_16x16x32_bf16 v[2:5], v[90:93], v[122:125], v[2:5]
	v_mfma_f32_16x16x32_bf16 v[62:65], v[70:73], v[102:105], v[62:65]
	v_mfma_f32_16x16x32_bf16 v[58:61], v[78:81], v[102:105], v[58:61]
	v_mfma_f32_16x16x32_bf16 v[54:57], v[70:73], v[110:113], v[54:57]
	v_mfma_f32_16x16x32_bf16 v[50:53], v[78:81], v[110:113], v[50:53]
	v_mfma_f32_16x16x32_bf16 v[38:41], v[70:73], v[118:121], v[38:41]
	v_mfma_f32_16x16x32_bf16 v[34:37], v[78:81], v[118:121], v[34:37]
	v_mfma_f32_16x16x32_bf16 v[22:25], v[70:73], v[126:129], v[22:25]
	v_mfma_f32_16x16x32_bf16 v[18:21], v[78:81], v[126:129], v[18:21]
	v_mfma_f32_16x16x32_bf16 v[46:49], v[86:89], v[102:105], v[46:49]
	v_mfma_f32_16x16x32_bf16 v[42:45], v[94:97], v[102:105], v[42:45]
	v_mfma_f32_16x16x32_bf16 v[30:33], v[86:89], v[110:113], v[30:33]
	v_mfma_f32_16x16x32_bf16 v[26:29], v[94:97], v[110:113], v[26:29]
	v_mfma_f32_16x16x32_bf16 v[14:17], v[86:89], v[118:121], v[14:17]
	v_mfma_f32_16x16x32_bf16 v[10:13], v[94:97], v[118:121], v[10:13]
	v_mfma_f32_16x16x32_bf16 v[6:9], v[86:89], v[126:129], v[6:9]
	v_mfma_f32_16x16x32_bf16 v[2:5], v[94:97], v[126:129], v[2:5]
	s_barrier
	s_mov_b32 m0, s61
	s_add_i32 s51, s47, 0x80
	buffer_load_dwordx4 v152, s[8:11], s51 offen lds
	s_mov_b32 m0, s62
	s_add_i32 s47, s47, 0x80080
	buffer_load_dwordx4 v154, s[8:11], s51 offen lds
	s_mov_b32 m0, s65
	s_addk_i32 s50, 0x80
	buffer_load_dwordx4 v152, s[8:11], s47 offen lds
	s_mov_b32 m0, s66
	s_nop 0
	buffer_load_dwordx4 v154, s[8:11], s47 offen lds
	s_mov_b32 m0, s63
	s_nop 0
	buffer_load_dwordx4 v1, s[4:7], s50 offen lds
	s_mov_b32 m0, s64
	s_nop 0
	buffer_load_dwordx4 v153, s[4:7], s50 offen lds
	s_waitcnt vmcnt(8)
	s_waitcnt lgkmcnt(0)
	s_barrier
	s_barrier
	s_add_i32 s45, s45, 2
	s_add_u32 s48, s48, 0x100
	s_addc_u32 s49, s49, 0
	s_cmp_lt_u32 s45, 30
	s_cbranch_scc1 .LBB0_1456
	s_mov_b64 s[10:11], 0

.LBB0_1460:
	ds_read_b128 v[132:135], v159
	ds_read_b128 v[136:139], v159 offset:1024
	ds_read_b128 v[140:143], v159 offset:2048
	ds_read_b128 v[164:167], v159 offset:3072
	ds_read_b128 v[168:171], v160
	ds_read_b128 v[172:175], v160 offset:1024
	ds_read_b128 v[176:179], v160 offset:2048
	ds_read_b128 v[180:183], v160 offset:3072
	s_add_i32 s10, s44, s48
	s_sub_i32 s10, s10, s4
	s_add_i32 s47, s46, s48
	s_add_i32 s10, s10, 0x7ff80
	s_cmp_eq_u32 s45, 28
	s_cselect_b32 s50, 0, s48
	s_mov_b32 m0, s67
	ds_read_b128 v[184:187], v161
	ds_read_b128 v[188:191], v161 offset:1024
	ds_read_b128 v[196:199], v161 offset:2048
	ds_read_b128 v[200:203], v161 offset:3072
	ds_read_b128 v[204:207], v161 offset:4096
	ds_read_b128 v[208:211], v161 offset:5120
	ds_read_b128 v[212:215], v161 offset:6144
	ds_read_b128 v[216:219], v161 offset:7168
	buffer_load_dwordx4 v1, s[4:7], s10 offen lds
	s_mov_b32 m0, s68
	s_nop 0
	buffer_load_dwordx4 v153, s[4:7], s10 offen lds
	s_waitcnt vmcnt(8)
	s_waitcnt lgkmcnt(0)
	s_barrier
	v_mfma_f32_16x16x32_bf16 v[62:65], v[132:135], v[184:187], v[62:65]
	v_mfma_f32_16x16x32_bf16 v[58:61], v[140:143], v[184:187], v[58:61]
	v_mfma_f32_16x16x32_bf16 v[54:57], v[132:135], v[196:199], v[54:57]
	v_mfma_f32_16x16x32_bf16 v[50:53], v[140:143], v[196:199], v[50:53]
	v_mfma_f32_16x16x32_bf16 v[38:41], v[132:135], v[204:207], v[38:41]
	v_mfma_f32_16x16x32_bf16 v[34:37], v[140:143], v[204:207], v[34:37]
	v_mfma_f32_16x16x32_bf16 v[22:25], v[132:135], v[212:215], v[22:25]
	v_mfma_f32_16x16x32_bf16 v[18:21], v[140:143], v[212:215], v[18:21]
	v_mfma_f32_16x16x32_bf16 v[46:49], v[168:171], v[184:187], v[46:49]
	v_mfma_f32_16x16x32_bf16 v[42:45], v[176:179], v[184:187], v[42:45]
	v_mfma_f32_16x16x32_bf16 v[30:33], v[168:171], v[196:199], v[30:33]
	v_mfma_f32_16x16x32_bf16 v[26:29], v[176:179], v[196:199], v[26:29]
	v_mfma_f32_16x16x32_bf16 v[14:17], v[168:171], v[204:207], v[14:17]
	v_mfma_f32_16x16x32_bf16 v[10:13], v[176:179], v[204:207], v[10:13]
	v_mfma_f32_16x16x32_bf16 v[6:9], v[168:171], v[212:215], v[6:9]
	v_mfma_f32_16x16x32_bf16 v[2:5], v[176:179], v[212:215], v[2:5]
	v_mfma_f32_16x16x32_bf16 v[62:65], v[136:139], v[188:191], v[62:65]
	v_mfma_f32_16x16x32_bf16 v[58:61], v[164:167], v[188:191], v[58:61]
	v_mfma_f32_16x16x32_bf16 v[54:57], v[136:139], v[200:203], v[54:57]
	v_mfma_f32_16x16x32_bf16 v[50:53], v[164:167], v[200:203], v[50:53]
	v_mfma_f32_16x16x32_bf16 v[38:41], v[136:139], v[208:211], v[38:41]
	v_mfma_f32_16x16x32_bf16 v[34:37], v[164:167], v[208:211], v[34:37]
	v_mfma_f32_16x16x32_bf16 v[22:25], v[136:139], v[216:219], v[22:25]
	v_mfma_f32_16x16x32_bf16 v[18:21], v[164:167], v[216:219], v[18:21]
	v_mfma_f32_16x16x32_bf16 v[46:49], v[172:175], v[188:191], v[46:49]
	v_mfma_f32_16x16x32_bf16 v[42:45], v[180:183], v[188:191], v[42:45]
	v_mfma_f32_16x16x32_bf16 v[30:33], v[172:175], v[200:203], v[30:33]
	v_mfma_f32_16x16x32_bf16 v[26:29], v[180:183], v[200:203], v[26:29]
	v_mfma_f32_16x16x32_bf16 v[14:17], v[172:175], v[208:211], v[14:17]
	v_mfma_f32_16x16x32_bf16 v[10:13], v[180:183], v[208:211], v[10:13]
	v_mfma_f32_16x16x32_bf16 v[6:9], v[172:175], v[216:219], v[6:9]
	v_mfma_f32_16x16x32_bf16 v[2:5], v[180:183], v[216:219], v[2:5]
	s_barrier
	s_cselect_b32 s47, s31, s47
	s_mov_b32 m0, s53
	s_mov_b32 s10, s6
	s_mov_b32 s11, s7
	s_cselect_b32 s51, s27, s44
	s_sub_i32 s47, s47, s8
	ds_read_b128 v[184:187], v161 offset:16384
	ds_read_b128 v[188:191], v161 offset:17408
	ds_read_b128 v[196:199], v161 offset:18432
	ds_read_b128 v[200:203], v161 offset:19456
	ds_read_b128 v[204:207], v161 offset:20480
	ds_read_b128 v[208:211], v161 offset:21504
	ds_read_b128 v[212:215], v161 offset:22528
	ds_read_b128 v[216:219], v161 offset:23552
	buffer_load_dwordx4 v152, s[8:11], s47 offen lds
	s_mov_b32 m0, s54
	s_add_i32 s73, s47, 0x80000
	buffer_load_dwordx4 v154, s[8:11], s47 offen lds
	s_mov_b32 m0, s55
	s_add_i32 s51, s51, s50
	buffer_load_dwordx4 v152, s[8:11], s73 offen lds
	s_mov_b32 m0, s56
	s_sub_i32 s50, s51, s4
	buffer_load_dwordx4 v154, s[8:11], s73 offen lds
	s_mov_b32 m0, s43
	s_nop 0
	buffer_load_dwordx4 v1, s[4:7], s50 offen lds
	s_mov_b32 m0, s57
	s_nop 0
	buffer_load_dwordx4 v153, s[4:7], s50 offen lds
	s_waitcnt vmcnt(8)
	s_waitcnt lgkmcnt(0)
	s_barrier
	v_mfma_f32_16x16x32_bf16 v[126:129], v[132:135], v[184:187], v[126:129]
	v_mfma_f32_16x16x32_bf16 v[122:125], v[140:143], v[184:187], v[122:125]
	v_mfma_f32_16x16x32_bf16 v[110:113], v[132:135], v[196:199], v[110:113]
	v_mfma_f32_16x16x32_bf16 v[106:109], v[140:143], v[196:199], v[106:109]
	v_mfma_f32_16x16x32_bf16 v[94:97], v[132:135], v[204:207], v[94:97]
	v_mfma_f32_16x16x32_bf16 v[90:93], v[140:143], v[204:207], v[90:93]
	v_mfma_f32_16x16x32_bf16 v[78:81], v[132:135], v[212:215], v[78:81]
	v_mfma_f32_16x16x32_bf16 v[74:77], v[140:143], v[212:215], v[74:77]
	v_mfma_f32_16x16x32_bf16 v[118:121], v[168:171], v[184:187], v[118:121]
	v_mfma_f32_16x16x32_bf16 v[114:117], v[176:179], v[184:187], v[114:117]
	v_mfma_f32_16x16x32_bf16 v[102:105], v[168:171], v[196:199], v[102:105]
	v_mfma_f32_16x16x32_bf16 v[98:101], v[176:179], v[196:199], v[98:101]
	v_mfma_f32_16x16x32_bf16 v[86:89], v[168:171], v[204:207], v[86:89]
	v_mfma_f32_16x16x32_bf16 v[82:85], v[176:179], v[204:207], v[82:85]
	v_mfma_f32_16x16x32_bf16 v[70:73], v[168:171], v[212:215], v[70:73]
	v_mfma_f32_16x16x32_bf16 v[66:69], v[176:179], v[212:215], v[66:69]
	v_mfma_f32_16x16x32_bf16 v[126:129], v[136:139], v[188:191], v[126:129]
	v_mfma_f32_16x16x32_bf16 v[122:125], v[164:167], v[188:191], v[122:125]
	v_mfma_f32_16x16x32_bf16 v[110:113], v[136:139], v[200:203], v[110:113]
	v_mfma_f32_16x16x32_bf16 v[106:109], v[164:167], v[200:203], v[106:109]
	v_mfma_f32_16x16x32_bf16 v[94:97], v[136:139], v[208:211], v[94:97]
	v_mfma_f32_16x16x32_bf16 v[90:93], v[164:167], v[208:211], v[90:93]
	v_mfma_f32_16x16x32_bf16 v[78:81], v[136:139], v[216:219], v[78:81]
	v_mfma_f32_16x16x32_bf16 v[74:77], v[164:167], v[216:219], v[74:77]
	v_mfma_f32_16x16x32_bf16 v[118:121], v[172:175], v[188:191], v[118:121]
	v_mfma_f32_16x16x32_bf16 v[114:117], v[180:183], v[188:191], v[114:117]
	v_mfma_f32_16x16x32_bf16 v[102:105], v[172:175], v[200:203], v[102:105]
	v_mfma_f32_16x16x32_bf16 v[98:101], v[180:183], v[200:203], v[98:101]
	v_mfma_f32_16x16x32_bf16 v[86:89], v[172:175], v[208:211], v[86:89]
	v_mfma_f32_16x16x32_bf16 v[82:85], v[180:183], v[208:211], v[82:85]
	v_mfma_f32_16x16x32_bf16 v[70:73], v[172:175], v[216:219], v[70:73]
	v_mfma_f32_16x16x32_bf16 v[66:69], v[180:183], v[216:219], v[66:69]
	s_barrier
	ds_read_b128 v[132:135], v162
	ds_read_b128 v[136:139], v162 offset:1024
	ds_read_b128 v[140:143], v162 offset:2048
	ds_read_b128 v[164:167], v162 offset:3072
	ds_read_b128 v[168:171], v163
	ds_read_b128 v[172:175], v163 offset:1024
	ds_read_b128 v[176:179], v163 offset:2048
	ds_read_b128 v[180:183], v163 offset:3072
	s_add_i32 s51, s50, 0x80000
	s_mov_b32 m0, s58
	ds_read_b128 v[184:187], v161 offset:32768
	ds_read_b128 v[188:191], v161 offset:33792
	ds_read_b128 v[196:199], v161 offset:34816
	ds_read_b128 v[200:203], v161 offset:35840
	ds_read_b128 v[204:207], v161 offset:36864
	ds_read_b128 v[208:211], v161 offset:37888
	ds_read_b128 v[212:215], v161 offset:38912
	ds_read_b128 v[216:219], v161 offset:39936
	buffer_load_dwordx4 v1, s[4:7], s51 offen lds
	s_mov_b32 m0, s59
	s_nop 0
	buffer_load_dwordx4 v153, s[4:7], s51 offen lds
	s_waitcnt vmcnt(8)
	s_waitcnt lgkmcnt(0)
	s_barrier
	v_mfma_f32_16x16x32_bf16 v[62:65], v[132:135], v[184:187], v[62:65]
	v_mfma_f32_16x16x32_bf16 v[58:61], v[140:143], v[184:187], v[58:61]
	v_mfma_f32_16x16x32_bf16 v[54:57], v[132:135], v[196:199], v[54:57]
	v_mfma_f32_16x16x32_bf16 v[50:53], v[140:143], v[196:199], v[50:53]
	v_mfma_f32_16x16x32_bf16 v[38:41], v[132:135], v[204:207], v[38:41]
	v_mfma_f32_16x16x32_bf16 v[34:37], v[140:143], v[204:207], v[34:37]
	v_mfma_f32_16x16x32_bf16 v[22:25], v[132:135], v[212:215], v[22:25]
	v_mfma_f32_16x16x32_bf16 v[18:21], v[140:143], v[212:215], v[18:21]
	v_mfma_f32_16x16x32_bf16 v[46:49], v[168:171], v[184:187], v[46:49]
	v_mfma_f32_16x16x32_bf16 v[42:45], v[176:179], v[184:187], v[42:45]
	v_mfma_f32_16x16x32_bf16 v[30:33], v[168:171], v[196:199], v[30:33]
	v_mfma_f32_16x16x32_bf16 v[26:29], v[176:179], v[196:199], v[26:29]
	v_mfma_f32_16x16x32_bf16 v[14:17], v[168:171], v[204:207], v[14:17]
	v_mfma_f32_16x16x32_bf16 v[10:13], v[176:179], v[204:207], v[10:13]
	v_mfma_f32_16x16x32_bf16 v[6:9], v[168:171], v[212:215], v[6:9]
	v_mfma_f32_16x16x32_bf16 v[2:5], v[176:179], v[212:215], v[2:5]
	v_mfma_f32_16x16x32_bf16 v[62:65], v[136:139], v[188:191], v[62:65]
	v_mfma_f32_16x16x32_bf16 v[58:61], v[164:167], v[188:191], v[58:61]
	v_mfma_f32_16x16x32_bf16 v[54:57], v[136:139], v[200:203], v[54:57]
	v_mfma_f32_16x16x32_bf16 v[50:53], v[164:167], v[200:203], v[50:53]
	v_mfma_f32_16x16x32_bf16 v[38:41], v[136:139], v[208:211], v[38:41]
	v_mfma_f32_16x16x32_bf16 v[34:37], v[164:167], v[208:211], v[34:37]
	v_mfma_f32_16x16x32_bf16 v[22:25], v[136:139], v[216:219], v[22:25]
	v_mfma_f32_16x16x32_bf16 v[18:21], v[164:167], v[216:219], v[18:21]
	v_mfma_f32_16x16x32_bf16 v[46:49], v[172:175], v[188:191], v[46:49]
	v_mfma_f32_16x16x32_bf16 v[42:45], v[180:183], v[188:191], v[42:45]
	v_mfma_f32_16x16x32_bf16 v[30:33], v[172:175], v[200:203], v[30:33]
	v_mfma_f32_16x16x32_bf16 v[26:29], v[180:183], v[200:203], v[26:29]
	v_mfma_f32_16x16x32_bf16 v[14:17], v[172:175], v[208:211], v[14:17]
	v_mfma_f32_16x16x32_bf16 v[10:13], v[180:183], v[208:211], v[10:13]
	v_mfma_f32_16x16x32_bf16 v[6:9], v[172:175], v[216:219], v[6:9]
	v_mfma_f32_16x16x32_bf16 v[2:5], v[180:183], v[216:219], v[2:5]
	s_barrier
	s_mov_b32 m0, s61
	s_add_i32 s51, s47, 0x80
	ds_read_b128 v[184:187], v161 offset:49152
	ds_read_b128 v[188:191], v161 offset:50176
	ds_read_b128 v[196:199], v161 offset:51200
	ds_read_b128 v[200:203], v161 offset:52224
	ds_read_b128 v[204:207], v161 offset:53248
	ds_read_b128 v[208:211], v161 offset:54272
	ds_read_b128 v[212:215], v161 offset:55296
	ds_read_b128 v[216:219], v161 offset:56320
	buffer_load_dwordx4 v152, s[8:11], s51 offen lds
	s_mov_b32 m0, s62
	s_add_i32 s47, s47, 0x80080
	buffer_load_dwordx4 v154, s[8:11], s51 offen lds
	s_mov_b32 m0, s65
	s_addk_i32 s50, 0x80
	buffer_load_dwordx4 v152, s[8:11], s47 offen lds
	s_mov_b32 m0, s66
	s_nop 0
	buffer_load_dwordx4 v154, s[8:11], s47 offen lds
	s_mov_b32 m0, s63
	s_nop 0
	buffer_load_dwordx4 v1, s[4:7], s50 offen lds
	s_mov_b32 m0, s64
	s_nop 0
	buffer_load_dwordx4 v153, s[4:7], s50 offen lds
	s_waitcnt vmcnt(8)
	s_waitcnt lgkmcnt(0)
	s_barrier
	v_mfma_f32_16x16x32_bf16 v[126:129], v[132:135], v[184:187], v[126:129]
	v_mfma_f32_16x16x32_bf16 v[122:125], v[140:143], v[184:187], v[122:125]
	v_mfma_f32_16x16x32_bf16 v[110:113], v[132:135], v[196:199], v[110:113]
	v_mfma_f32_16x16x32_bf16 v[106:109], v[140:143], v[196:199], v[106:109]
	v_mfma_f32_16x16x32_bf16 v[94:97], v[132:135], v[204:207], v[94:97]
	v_mfma_f32_16x16x32_bf16 v[90:93], v[140:143], v[204:207], v[90:93]
	v_mfma_f32_16x16x32_bf16 v[78:81], v[132:135], v[212:215], v[78:81]
	v_mfma_f32_16x16x32_bf16 v[74:77], v[140:143], v[212:215], v[74:77]
	v_mfma_f32_16x16x32_bf16 v[118:121], v[168:171], v[184:187], v[118:121]
	v_mfma_f32_16x16x32_bf16 v[114:117], v[176:179], v[184:187], v[114:117]
	v_mfma_f32_16x16x32_bf16 v[102:105], v[168:171], v[196:199], v[102:105]
	v_mfma_f32_16x16x32_bf16 v[98:101], v[176:179], v[196:199], v[98:101]
	v_mfma_f32_16x16x32_bf16 v[86:89], v[168:171], v[204:207], v[86:89]
	v_mfma_f32_16x16x32_bf16 v[82:85], v[176:179], v[204:207], v[82:85]
	v_mfma_f32_16x16x32_bf16 v[70:73], v[168:171], v[212:215], v[70:73]
	v_mfma_f32_16x16x32_bf16 v[66:69], v[176:179], v[212:215], v[66:69]
	v_mfma_f32_16x16x32_bf16 v[126:129], v[136:139], v[188:191], v[126:129]
	v_mfma_f32_16x16x32_bf16 v[122:125], v[164:167], v[188:191], v[122:125]
	v_mfma_f32_16x16x32_bf16 v[110:113], v[136:139], v[200:203], v[110:113]
	v_mfma_f32_16x16x32_bf16 v[106:109], v[164:167], v[200:203], v[106:109]
	v_mfma_f32_16x16x32_bf16 v[94:97], v[136:139], v[208:211], v[94:97]
	v_mfma_f32_16x16x32_bf16 v[90:93], v[164:167], v[208:211], v[90:93]
	v_mfma_f32_16x16x32_bf16 v[78:81], v[136:139], v[216:219], v[78:81]
	v_mfma_f32_16x16x32_bf16 v[74:77], v[164:167], v[216:219], v[74:77]
	v_mfma_f32_16x16x32_bf16 v[118:121], v[172:175], v[188:191], v[118:121]
	v_mfma_f32_16x16x32_bf16 v[114:117], v[180:183], v[188:191], v[114:117]
	v_mfma_f32_16x16x32_bf16 v[102:105], v[172:175], v[200:203], v[102:105]
	v_mfma_f32_16x16x32_bf16 v[98:101], v[180:183], v[200:203], v[98:101]
	v_mfma_f32_16x16x32_bf16 v[86:89], v[172:175], v[208:211], v[86:89]
	v_mfma_f32_16x16x32_bf16 v[82:85], v[180:183], v[208:211], v[82:85]
	v_mfma_f32_16x16x32_bf16 v[70:73], v[172:175], v[216:219], v[70:73]
	v_mfma_f32_16x16x32_bf16 v[66:69], v[180:183], v[216:219], v[66:69]
	s_barrier
	s_add_i32 s45, s45, 2
	s_add_u32 s48, s48, 0x100
	s_addc_u32 s49, s49, 0
	s_cmp_gt_u32 s45, 29
	s_cbranch_scc0 .LBB0_1460
